# v053 + five GEMM K-loops fully in saddr LDS-DMA form (scalar snapshot base+128 for the second K-tile): 80 64-bit vector adds dropped
# baseline (speedup 1.0000x reference)
; #define PG8_STAGE(bufoff, gbase, voff) do { _Pragma("unroll") for (int _i = 0; _i < 2; ++_i) \
;         __builtin_amdgcn_global_load_lds((const unsigned*)((const char*)(gbase) + (voff)[_i]), (LAS unsigned*)(lds + (bufoff) + ldsw + _i * 8192), 16, 0, 0); } while (0)
; #define PG8_LDA(dst, b, h) do { _Pragma("unroll") for (int m = 0; m < 4; ++m) _Pragma("unroll") for (int k = 0; k < 2; ++k) dst[m][k] = *(const LAS bf16x8*)(lds + PG8_SA(b, h) + aoff + m * 2048 + k * 1024); } while (0)
; #define PG8_LDB(dst, b, h) do { _Pragma("unroll") for (int n = 0; n < 2; ++n) _Pragma("unroll") for (int k = 0; k < 2; ++k) dst[n][k] = *(const LAS bf16x8*)(lds + PG8_SB(b, h) + boff + n * 2048 + k * 1024); } while (0)
; #define PG8_MMA(ai, bj, At, Bt_) do { __builtin_amdgcn_s_setprio(1); _Pragma("unroll") for (int m = 0; m < 4; ++m) _Pragma("unroll") for (int n = 0; n < 2; ++n) _Pragma("unroll") for (int k = 0; k < 2; ++k) \
;         acc[ai][bj][m][n] = __builtin_amdgcn_mfma_f32_16x16x32_bf16(Bt_[n][k], At[m][k], acc[ai][bj][m][n], 0, 0, 0); __builtin_amdgcn_s_setprio(0); } while (0)
; #define PG8_WAIT_L(n) asm volatile("s_waitcnt lgkmcnt(" #n ")" ::: "memory")
; #define PG8_WAIT_VR(rl) asm volatile("s_cmp_lg_u32 %0, 0\n\ts_cbranch_scc1 .Lwvr%=\n\ts_waitcnt vmcnt(8)\n.Lwvr%=:\n\ts_waitcnt vmcnt(24)" :: "s"(rl) : "scc", "memory")
; #define PG8_BAR __builtin_amdgcn_s_barrier()
; #define PG8_SCHED __builtin_amdgcn_sched_barrier(0)
; template <class Epi, class Sched, bool GATHER>
; __device__ __forceinline__ void gemm_phase(LAS unsigned char* lds, const int wid, const bf16_t* A, int lda, const bf16_t* Bt, int ldb, size_t b_estride, int K, const Sched& S, const Epi& E) {
;     ...
;             PG8_WAIT_VR(rl); PG8_WAIT_L(0); PG8_BAR; PG8_MMA(0, 0, At, B0); PG8_MMA(0, 1, At, B1); PG8_BAR; PG8_SCHED;
;             PG8_LDA(At, 0, 1); PG8_STAGE(PG8_SB(0, 0), b2, voffB); PG8_STAGE(PG8_SB(0, 1), b2 + hstepB, voffB); PG8_STAGE_A(PG8_SA(0, 0), a2, 0, k2, g20);
;             PG8_WAIT_VR(rl); PG8_WAIT_L(0); PG8_BAR; PG8_MMA(1, 0, At, B0); PG8_MMA(1, 1, At, B1); PG8_BAR; PG8_SCHED;
;             PG8_LDB(B0, 1, 0); PG8_LDB(B1, 1, 1); PG8_SCHED; PG8_LDA(At, 1, 0); PG8_STAGE_A(PG8_SA(0, 1), a2, 1, k2, g21);
.Lwvr0:
	s_waitcnt vmcnt(24)
	s_waitcnt lgkmcnt(0)
	s_barrier
	s_setprio 1
	s_waitcnt lgkmcnt(0)
	v_mfma_f32_16x16x32_bf16 v[124:127], v[128:131], v[182:185], v[124:127]
	v_mfma_f32_16x16x32_bf16 v[120:123], v[136:139], v[182:185], v[120:123]
	v_mfma_f32_16x16x32_bf16 v[108:111], v[128:131], v[190:193], v[108:111]
	v_mfma_f32_16x16x32_bf16 v[104:107], v[136:139], v[190:193], v[104:107]
	v_mfma_f32_16x16x32_bf16 v[92:95], v[128:131], v[200:203], v[92:95]
	v_mfma_f32_16x16x32_bf16 v[88:91], v[136:139], v[200:203], v[88:91]
	v_mfma_f32_16x16x32_bf16 v[76:79], v[128:131], v[208:211], v[76:79]
	v_mfma_f32_16x16x32_bf16 v[72:75], v[136:139], v[208:211], v[72:75]
	v_mfma_f32_16x16x32_bf16 v[124:127], v[132:135], v[186:189], v[124:127]
	v_mfma_f32_16x16x32_bf16 v[120:123], v[140:143], v[186:189], v[120:123]
	v_mfma_f32_16x16x32_bf16 v[108:111], v[132:135], v[194:197], v[108:111]
	v_mfma_f32_16x16x32_bf16 v[104:107], v[140:143], v[194:197], v[104:107]
	v_mfma_f32_16x16x32_bf16 v[92:95], v[132:135], v[204:207], v[92:95]
	v_mfma_f32_16x16x32_bf16 v[88:91], v[140:143], v[204:207], v[88:91]
	v_mfma_f32_16x16x32_bf16 v[76:79], v[132:135], v[212:215], v[76:79]
	v_mfma_f32_16x16x32_bf16 v[72:75], v[140:143], v[212:215], v[72:75]
	s_setprio 0
	s_setprio 1
	v_mfma_f32_16x16x32_bf16 v[116:119], v[144:147], v[182:185], v[116:119]
	v_mfma_f32_16x16x32_bf16 v[112:115], v[166:169], v[182:185], v[112:115]
	v_mfma_f32_16x16x32_bf16 v[100:103], v[144:147], v[190:193], v[100:103]
	v_mfma_f32_16x16x32_bf16 v[96:99], v[166:169], v[190:193], v[96:99]
	v_mfma_f32_16x16x32_bf16 v[84:87], v[144:147], v[200:203], v[84:87]
	v_mfma_f32_16x16x32_bf16 v[80:83], v[166:169], v[200:203], v[80:83]
	v_mfma_f32_16x16x32_bf16 v[68:71], v[144:147], v[208:211], v[68:71]
	v_mfma_f32_16x16x32_bf16 v[64:67], v[166:169], v[208:211], v[64:67]
	v_mfma_f32_16x16x32_bf16 v[116:119], v[148:151], v[186:189], v[116:119]
	v_mfma_f32_16x16x32_bf16 v[112:115], v[170:173], v[186:189], v[112:115]
	v_mfma_f32_16x16x32_bf16 v[100:103], v[148:151], v[194:197], v[100:103]
	v_mfma_f32_16x16x32_bf16 v[96:99], v[170:173], v[194:197], v[96:99]
	v_mfma_f32_16x16x32_bf16 v[84:87], v[148:151], v[204:207], v[84:87]
	v_mfma_f32_16x16x32_bf16 v[80:83], v[170:173], v[204:207], v[80:83]
	v_mfma_f32_16x16x32_bf16 v[68:71], v[148:151], v[212:215], v[68:71]
	v_mfma_f32_16x16x32_bf16 v[64:67], v[170:173], v[212:215], v[64:67]
	s_setprio 0
	s_barrier
	s_add_i32 s96, s87, s33
	s_add_u32 s98, s70, 0x80
	s_addc_u32 s99, s71, 0
	s_mov_b32 m0, s96
	ds_read_b128 v[182:185], v177 offset:16384
	ds_read_b128 v[186:189], v177 offset:17408
	ds_read_b128 v[190:193], v177 offset:18432
	ds_read_b128 v[194:197], v177 offset:19456
	ds_read_b128 v[200:203], v177 offset:20480
	ds_read_b128 v[204:207], v177 offset:21504
	ds_read_b128 v[208:211], v177 offset:22528
	ds_read_b128 v[212:215], v177 offset:23552
	global_load_lds_dwordx4 v154, s[70:71]
	s_add_i32 m0, s96, 0x2000
	s_add_u32 s96, s70, 0x40000
	s_addc_u32 s97, s71, 0
	s_add_i32 vcc_lo, s88, s33
	global_load_lds_dwordx4 v158, s[70:71]
	s_mov_b32 m0, vcc_lo
	s_add_u32 s100, s60, 0x80
	s_addc_u32 s101, s61, 0
	global_load_lds_dwordx4 v154, s[96:97]
	s_add_i32 m0, vcc_lo, 0x2000
	s_nop 0
	global_load_lds_dwordx4 v158, s[96:97]
	s_mov_b32 m0, s15
	s_nop 0
	global_load_lds_dwordx4 v152, s[60:61]
	s_mov_b32 m0, s74
	s_nop 0
	global_load_lds_dwordx4 v156, s[60:61]
	s_cmp_lg_u32 s95, 0
	s_cbranch_scc1 .Lwvr1
	s_waitcnt vmcnt(8)
.Lwvr1:
	s_waitcnt vmcnt(24)
	s_waitcnt lgkmcnt(0)
	s_barrier
	s_setprio 1
	s_waitcnt lgkmcnt(0)
	v_mfma_f32_16x16x32_bf16 v[60:63], v[128:131], v[182:185], v[60:63]
	v_mfma_f32_16x16x32_bf16 v[56:59], v[136:139], v[182:185], v[56:59]
	v_mfma_f32_16x16x32_bf16 v[44:47], v[128:131], v[190:193], v[44:47]
	v_mfma_f32_16x16x32_bf16 v[40:43], v[136:139], v[190:193], v[40:43]
	v_mfma_f32_16x16x32_bf16 v[28:31], v[128:131], v[200:203], v[28:31]
	v_mfma_f32_16x16x32_bf16 v[24:27], v[136:139], v[200:203], v[24:27]
	v_mfma_f32_16x16x32_bf16 v[12:15], v[128:131], v[208:211], v[12:15]
	v_mfma_f32_16x16x32_bf16 v[8:11], v[136:139], v[208:211], v[8:11]
	v_mfma_f32_16x16x32_bf16 v[60:63], v[132:135], v[186:189], v[60:63]
	v_mfma_f32_16x16x32_bf16 v[56:59], v[140:143], v[186:189], v[56:59]
	v_mfma_f32_16x16x32_bf16 v[44:47], v[132:135], v[194:197], v[44:47]
	v_mfma_f32_16x16x32_bf16 v[40:43], v[140:143], v[194:197], v[40:43]
	v_mfma_f32_16x16x32_bf16 v[28:31], v[132:135], v[204:207], v[28:31]
	v_mfma_f32_16x16x32_bf16 v[24:27], v[140:143], v[204:207], v[24:27]
	v_mfma_f32_16x16x32_bf16 v[12:15], v[132:135], v[212:215], v[12:15]
	v_mfma_f32_16x16x32_bf16 v[8:11], v[140:143], v[212:215], v[8:11]
	s_setprio 0
	s_setprio 1
	v_mfma_f32_16x16x32_bf16 v[52:55], v[144:147], v[182:185], v[52:55]
	v_mfma_f32_16x16x32_bf16 v[48:51], v[166:169], v[182:185], v[48:51]
	v_mfma_f32_16x16x32_bf16 v[36:39], v[144:147], v[190:193], v[36:39]
	v_mfma_f32_16x16x32_bf16 v[32:35], v[166:169], v[190:193], v[32:35]
	v_mfma_f32_16x16x32_bf16 v[20:23], v[144:147], v[200:203], v[20:23]
	v_mfma_f32_16x16x32_bf16 v[16:19], v[166:169], v[200:203], v[16:19]
	v_mfma_f32_16x16x32_bf16 v[4:7], v[144:147], v[208:211], v[4:7]
	v_mfma_f32_16x16x32_bf16 v[0:3], v[166:169], v[208:211], v[0:3]
	v_mfma_f32_16x16x32_bf16 v[52:55], v[148:151], v[186:189], v[52:55]
	v_mfma_f32_16x16x32_bf16 v[48:51], v[170:173], v[186:189], v[48:51]
	v_mfma_f32_16x16x32_bf16 v[36:39], v[148:151], v[194:197], v[36:39]
	v_mfma_f32_16x16x32_bf16 v[32:35], v[170:173], v[194:197], v[32:35]
	v_mfma_f32_16x16x32_bf16 v[20:23], v[148:151], v[204:207], v[20:23]
	v_mfma_f32_16x16x32_bf16 v[16:19], v[170:173], v[204:207], v[16:19]
	v_mfma_f32_16x16x32_bf16 v[4:7], v[148:151], v[212:215], v[4:7]
	v_mfma_f32_16x16x32_bf16 v[0:3], v[170:173], v[212:215], v[0:3]
	s_setprio 0
	s_barrier
	s_add_i32 vcc_lo, 0, 0x18000
	s_add_i32 vcc_hi, 0, 0x1c000
	v_add_u32_e32 v140, vcc_lo, v174
	v_add_u32_e32 v160, vcc_hi, v174
	ds_read_b128 v[128:131], v140
	ds_read_b128 v[132:135], v140 offset:1024
	ds_read_b128 v[136:139], v140 offset:2048
	ds_read_b128 v[140:143], v140 offset:3072
	ds_read_b128 v[144:147], v160
	ds_read_b128 v[148:151], v160 offset:1024
	ds_read_b128 v[166:169], v160 offset:2048
	ds_read_b128 v[170:173], v160 offset:3072
	s_add_u32 s96, s60, 0x40000
	s_addc_u32 s97, s61, 0
	s_mov_b32 m0, s75
	ds_read_b128 v[182:185], v177 offset:32768
	ds_read_b128 v[186:189], v177 offset:33792
	ds_read_b128 v[190:193], v177 offset:34816
	ds_read_b128 v[194:197], v177 offset:35840
	ds_read_b128 v[200:203], v177 offset:36864
	ds_read_b128 v[204:207], v177 offset:37888
	ds_read_b128 v[208:211], v177 offset:38912
	ds_read_b128 v[212:215], v177 offset:39936
	global_load_lds_dwordx4 v152, s[96:97]
	s_mov_b32 m0, s76
	s_nop 0
	global_load_lds_dwordx4 v156, s[96:97]
	s_cmp_lg_u32 s95, 0
	s_cbranch_scc1 .Lwvr2
	s_waitcnt vmcnt(8)
; #define PG8_STAGE(bufoff, gbase, voff) do { _Pragma("unroll") for (int _i = 0; _i < 2; ++_i) \
;         __builtin_amdgcn_global_load_lds((const unsigned*)((const char*)(gbase) + (voff)[_i]), (LAS unsigned*)(lds + (bufoff) + ldsw + _i * 8192), 16, 0, 0); } while (0)
; #define PG8_LDA(dst, b, h) do { _Pragma("unroll") for (int m = 0; m < 4; ++m) _Pragma("unroll") for (int k = 0; k < 2; ++k) dst[m][k] = *(const LAS bf16x8*)(lds + PG8_SA(b, h) + aoff + m * 2048 + k * 1024); } while (0)
; #define PG8_MMA(ai, bj, At, Bt_) do { __builtin_amdgcn_s_setprio(1); _Pragma("unroll") for (int m = 0; m < 4; ++m) _Pragma("unroll") for (int n = 0; n < 2; ++n) _Pragma("unroll") for (int k = 0; k < 2; ++k) \
;         acc[ai][bj][m][n] = __builtin_amdgcn_mfma_f32_16x16x32_bf16(Bt_[n][k], At[m][k], acc[ai][bj][m][n], 0, 0, 0); __builtin_amdgcn_s_setprio(0); } while (0)
; #define PG8_WAIT_V(n) asm volatile("s_waitcnt vmcnt(" #n ")" ::: "memory")
; #define PG8_WAIT_L(n) asm volatile("s_waitcnt lgkmcnt(" #n ")" ::: "memory")
; #define PG8_WAIT_VR(rl) asm volatile("s_cmp_lg_u32 %0, 0\n\ts_cbranch_scc1 .Lwvr%=\n\ts_waitcnt vmcnt(8)\n.Lwvr%=:\n\ts_waitcnt vmcnt(24)" :: "s"(rl) : "scc", "memory")
; #define PG8_BAR __builtin_amdgcn_s_barrier()
; #define PG8_SCHED __builtin_amdgcn_sched_barrier(0)
; #define PG8_STAGE_A(bufoff, ptr_dense, half, ktoff, goffs) do { if constexpr (GATHER) { PG8_STAGE(bufoff, (const char*)A + (ktoff), goffs); } \
;         else { PG8_STAGE(bufoff, (ptr_dense) + (half) * hstepA, voffA); } } while (0)
; template <class Epi, class Sched, bool GATHER>
; __device__ __forceinline__ void gemm_phase(LAS unsigned char* lds, const int wid, const bf16_t* A, int lda, const bf16_t* Bt, int ldb, size_t b_estride, int K, const Sched& S, const Epi& E) {
;     ...
;             PG8_WAIT_VR(rl); PG8_WAIT_L(0); PG8_BAR; PG8_MMA(0, 0, At, B0); PG8_MMA(0, 1, At, B1); PG8_BAR; PG8_SCHED;
;             PG8_LDA(At, 1, 1); PG8_STAGE(PG8_SB(1, 0), b3, voffB); PG8_STAGE(PG8_SB(1, 1), b3 + hstepB, voffB); PG8_STAGE_A(PG8_SA(1, 0), a3, 0, k3, g20);
;             PG8_WAIT_V(8); PG8_WAIT_L(0); PG8_BAR; PG8_MMA(1, 0, At, B0); PG8_MMA(1, 1, At, B1); PG8_BAR; PG8_SCHED;
;             PG8_STAGE_A(PG8_SA(1, 1), a3, 1, k3, g21);
;         }
.Lwvr2:
	s_waitcnt vmcnt(24)
	s_waitcnt lgkmcnt(0)
	s_barrier
	s_setprio 1
	s_waitcnt lgkmcnt(0)
	v_mfma_f32_16x16x32_bf16 v[124:127], v[128:131], v[182:185], v[124:127]
	v_mfma_f32_16x16x32_bf16 v[120:123], v[136:139], v[182:185], v[120:123]
	v_mfma_f32_16x16x32_bf16 v[108:111], v[128:131], v[190:193], v[108:111]
	v_mfma_f32_16x16x32_bf16 v[104:107], v[136:139], v[190:193], v[104:107]
	v_mfma_f32_16x16x32_bf16 v[92:95], v[128:131], v[200:203], v[92:95]
	v_mfma_f32_16x16x32_bf16 v[88:91], v[136:139], v[200:203], v[88:91]
	v_mfma_f32_16x16x32_bf16 v[76:79], v[128:131], v[208:211], v[76:79]
	v_mfma_f32_16x16x32_bf16 v[72:75], v[136:139], v[208:211], v[72:75]
	v_mfma_f32_16x16x32_bf16 v[124:127], v[132:135], v[186:189], v[124:127]
	v_mfma_f32_16x16x32_bf16 v[120:123], v[140:143], v[186:189], v[120:123]
	v_mfma_f32_16x16x32_bf16 v[108:111], v[132:135], v[194:197], v[108:111]
	v_mfma_f32_16x16x32_bf16 v[104:107], v[140:143], v[194:197], v[104:107]
	v_mfma_f32_16x16x32_bf16 v[92:95], v[132:135], v[204:207], v[92:95]
	v_mfma_f32_16x16x32_bf16 v[88:91], v[140:143], v[204:207], v[88:91]
	v_mfma_f32_16x16x32_bf16 v[76:79], v[132:135], v[212:215], v[76:79]
	v_mfma_f32_16x16x32_bf16 v[72:75], v[140:143], v[212:215], v[72:75]
	s_setprio 0
	s_setprio 1
	v_mfma_f32_16x16x32_bf16 v[116:119], v[144:147], v[182:185], v[116:119]
	v_mfma_f32_16x16x32_bf16 v[112:115], v[166:169], v[182:185], v[112:115]
	v_mfma_f32_16x16x32_bf16 v[100:103], v[144:147], v[190:193], v[100:103]
	v_mfma_f32_16x16x32_bf16 v[96:99], v[166:169], v[190:193], v[96:99]
	v_mfma_f32_16x16x32_bf16 v[84:87], v[144:147], v[200:203], v[84:87]
	v_mfma_f32_16x16x32_bf16 v[80:83], v[166:169], v[200:203], v[80:83]
	v_mfma_f32_16x16x32_bf16 v[68:71], v[144:147], v[208:211], v[68:71]
	v_mfma_f32_16x16x32_bf16 v[64:67], v[166:169], v[208:211], v[64:67]
	v_mfma_f32_16x16x32_bf16 v[116:119], v[148:151], v[186:189], v[116:119]
	v_mfma_f32_16x16x32_bf16 v[112:115], v[170:173], v[186:189], v[112:115]
	v_mfma_f32_16x16x32_bf16 v[100:103], v[148:151], v[194:197], v[100:103]
	v_mfma_f32_16x16x32_bf16 v[96:99], v[170:173], v[194:197], v[96:99]
	v_mfma_f32_16x16x32_bf16 v[84:87], v[148:151], v[204:207], v[84:87]
	v_mfma_f32_16x16x32_bf16 v[80:83], v[170:173], v[204:207], v[80:83]
	v_mfma_f32_16x16x32_bf16 v[68:71], v[148:151], v[212:215], v[68:71]
	v_mfma_f32_16x16x32_bf16 v[64:67], v[170:173], v[212:215], v[64:67]
	s_setprio 0
	s_barrier
	s_add_i32 s95, vcc_lo, s33
	s_mov_b32 m0, s95
	ds_read_b128 v[182:185], v177 offset:49152
	ds_read_b128 v[186:189], v177 offset:50176
	ds_read_b128 v[190:193], v177 offset:51200
	ds_read_b128 v[194:197], v177 offset:52224
	ds_read_b128 v[200:203], v177 offset:53248
	ds_read_b128 v[204:207], v177 offset:54272
	ds_read_b128 v[208:211], v177 offset:55296
	ds_read_b128 v[212:215], v177 offset:56320
	global_load_lds_dwordx4 v154, s[98:99]
	s_add_i32 m0, s95, 0x2000
	s_add_u32 s70, s70, 0x40080
	s_addc_u32 s71, s71, 0
	s_add_i32 s95, vcc_hi, s33
	global_load_lds_dwordx4 v158, s[98:99]
	s_mov_b32 m0, s95
	s_nop 0
	global_load_lds_dwordx4 v154, s[70:71]
	s_add_i32 m0, s95, 0x2000
	s_nop 0
	global_load_lds_dwordx4 v158, s[70:71]
	s_mov_b32 m0, s81
	s_nop 0
	global_load_lds_dwordx4 v152, s[100:101]
	s_mov_b32 m0, s82
	s_nop 0
	global_load_lds_dwordx4 v156, s[100:101]
	s_waitcnt vmcnt(8)
	s_waitcnt lgkmcnt(0)
	s_barrier
	s_setprio 1
	s_waitcnt lgkmcnt(0)
	v_mfma_f32_16x16x32_bf16 v[60:63], v[128:131], v[182:185], v[60:63]
	v_mfma_f32_16x16x32_bf16 v[56:59], v[136:139], v[182:185], v[56:59]
	v_mfma_f32_16x16x32_bf16 v[44:47], v[128:131], v[190:193], v[44:47]
	v_mfma_f32_16x16x32_bf16 v[40:43], v[136:139], v[190:193], v[40:43]
	v_mfma_f32_16x16x32_bf16 v[28:31], v[128:131], v[200:203], v[28:31]
	v_mfma_f32_16x16x32_bf16 v[24:27], v[136:139], v[200:203], v[24:27]
	v_mfma_f32_16x16x32_bf16 v[12:15], v[128:131], v[208:211], v[12:15]
	v_mfma_f32_16x16x32_bf16 v[8:11], v[136:139], v[208:211], v[8:11]
	v_mfma_f32_16x16x32_bf16 v[60:63], v[132:135], v[186:189], v[60:63]
	v_mfma_f32_16x16x32_bf16 v[56:59], v[140:143], v[186:189], v[56:59]
	v_mfma_f32_16x16x32_bf16 v[44:47], v[132:135], v[194:197], v[44:47]
	v_mfma_f32_16x16x32_bf16 v[40:43], v[140:143], v[194:197], v[40:43]
	v_mfma_f32_16x16x32_bf16 v[28:31], v[132:135], v[204:207], v[28:31]
	v_mfma_f32_16x16x32_bf16 v[24:27], v[140:143], v[204:207], v[24:27]
	v_mfma_f32_16x16x32_bf16 v[12:15], v[132:135], v[212:215], v[12:15]
	v_mfma_f32_16x16x32_bf16 v[8:11], v[140:143], v[212:215], v[8:11]
	s_setprio 0
	s_setprio 1
	v_mfma_f32_16x16x32_bf16 v[52:55], v[144:147], v[182:185], v[52:55]
	v_mfma_f32_16x16x32_bf16 v[48:51], v[166:169], v[182:185], v[48:51]
	v_mfma_f32_16x16x32_bf16 v[36:39], v[144:147], v[190:193], v[36:39]
	v_mfma_f32_16x16x32_bf16 v[32:35], v[166:169], v[190:193], v[32:35]
	v_mfma_f32_16x16x32_bf16 v[20:23], v[144:147], v[200:203], v[20:23]
	v_mfma_f32_16x16x32_bf16 v[16:19], v[166:169], v[200:203], v[16:19]
	v_mfma_f32_16x16x32_bf16 v[4:7], v[144:147], v[208:211], v[4:7]
	v_mfma_f32_16x16x32_bf16 v[0:3], v[166:169], v[208:211], v[0:3]
	v_mfma_f32_16x16x32_bf16 v[52:55], v[148:151], v[186:189], v[52:55]
	v_mfma_f32_16x16x32_bf16 v[48:51], v[170:173], v[186:189], v[48:51]
	v_mfma_f32_16x16x32_bf16 v[36:39], v[148:151], v[194:197], v[36:39]
	v_mfma_f32_16x16x32_bf16 v[32:35], v[170:173], v[194:197], v[32:35]
	v_mfma_f32_16x16x32_bf16 v[20:23], v[148:151], v[204:207], v[20:23]
	v_mfma_f32_16x16x32_bf16 v[16:19], v[170:173], v[204:207], v[16:19]
	v_mfma_f32_16x16x32_bf16 v[4:7], v[148:151], v[212:215], v[4:7]
	v_mfma_f32_16x16x32_bf16 v[0:3], v[170:173], v[212:215], v[0:3]
	s_setprio 0
	s_barrier
	s_add_u32 s60, s60, 0x40080
	s_addc_u32 s61, s61, 0
	s_mov_b32 m0, s83
	s_nop 0
	global_load_lds_dwordx4 v152, s[60:61]
	s_mov_b32 m0, s84
	s_add_i32 s94, s94, 2
	global_load_lds_dwordx4 v156, s[60:61]
	s_add_u32 s52, s52, 0x100
	s_addc_u32 s53, s53, 0
	s_add_u32 s92, s92, 0x100
	s_addc_u32 s93, s93, 0
	s_cmp_gt_u32 s94, 13
	s_cbranch_scc0 .LBB0_268
	s_and_b64 vcc, exec, s[40:41]
	s_cbranch_vccz .LBB0_271
	s_barrier

; #define PG8_STAGE(bufoff, gbase, voff) do { _Pragma("unroll") for (int _i = 0; _i < 2; ++_i) \
;         __builtin_amdgcn_global_load_lds((const unsigned*)((const char*)(gbase) + (voff)[_i]), (LAS unsigned*)(lds + (bufoff) + ldsw + _i * 8192), 16, 0, 0); } while (0)
; #define PG8_LDA(dst, b, h) do { _Pragma("unroll") for (int m = 0; m < 4; ++m) _Pragma("unroll") for (int k = 0; k < 2; ++k) dst[m][k] = *(const LAS bf16x8*)(lds + PG8_SA(b, h) + aoff + m * 2048 + k * 1024); } while (0)
; #define PG8_LDB(dst, b, h) do { _Pragma("unroll") for (int n = 0; n < 2; ++n) _Pragma("unroll") for (int k = 0; k < 2; ++k) dst[n][k] = *(const LAS bf16x8*)(lds + PG8_SB(b, h) + boff + n * 2048 + k * 1024); } while (0)
; #define PG8_MMA(ai, bj, At, Bt_) do { __builtin_amdgcn_s_setprio(1); _Pragma("unroll") for (int m = 0; m < 4; ++m) _Pragma("unroll") for (int n = 0; n < 2; ++n) _Pragma("unroll") for (int k = 0; k < 2; ++k) \
;         acc[ai][bj][m][n] = __builtin_amdgcn_mfma_f32_16x16x32_bf16(Bt_[n][k], At[m][k], acc[ai][bj][m][n], 0, 0, 0); __builtin_amdgcn_s_setprio(0); } while (0)
; #define PG8_WAIT_L(n) asm volatile("s_waitcnt lgkmcnt(" #n ")" ::: "memory")
; #define PG8_WAIT_VR(rl) asm volatile("s_cmp_lg_u32 %0, 0\n\ts_cbranch_scc1 .Lwvr%=\n\ts_waitcnt vmcnt(8)\n.Lwvr%=:\n\ts_waitcnt vmcnt(24)" :: "s"(rl) : "scc", "memory")
; #define PG8_BAR __builtin_amdgcn_s_barrier()
; #define PG8_SCHED __builtin_amdgcn_sched_barrier(0)
; template <class Epi, class Sched, bool GATHER>
; __device__ __forceinline__ void gemm_phase(LAS unsigned char* lds, const int wid, const bf16_t* A, int lda, const bf16_t* Bt, int ldb, size_t b_estride, int K, const Sched& S, const Epi& E) {
;     ...
;             PG8_WAIT_VR(rl); PG8_WAIT_L(0); PG8_BAR; PG8_MMA(0, 0, At, B0); PG8_MMA(0, 1, At, B1); PG8_BAR; PG8_SCHED;
;             PG8_LDA(At, 0, 1); PG8_STAGE(PG8_SB(0, 0), b2, voffB); PG8_STAGE(PG8_SB(0, 1), b2 + hstepB, voffB); PG8_STAGE_A(PG8_SA(0, 0), a2, 0, k2, g20);
;             PG8_WAIT_VR(rl); PG8_WAIT_L(0); PG8_BAR; PG8_MMA(1, 0, At, B0); PG8_MMA(1, 1, At, B1); PG8_BAR; PG8_SCHED;
;             PG8_LDB(B0, 1, 0); PG8_LDB(B1, 1, 1); PG8_SCHED; PG8_LDA(At, 1, 0); PG8_STAGE_A(PG8_SA(0, 1), a2, 1, k2, g21);
.Lwvr3:
	s_waitcnt vmcnt(24)
	s_waitcnt lgkmcnt(0)
	s_barrier
	s_setprio 1
	s_waitcnt lgkmcnt(0)
	v_mfma_f32_16x16x32_bf16 v[132:135], v[104:107], v[174:177], v[132:135]
	v_mfma_f32_16x16x32_bf16 v[128:131], v[136:139], v[174:177], v[128:131]
	v_mfma_f32_16x16x32_bf16 v[112:115], v[104:107], v[182:185], v[112:115]
	v_mfma_f32_16x16x32_bf16 v[108:111], v[136:139], v[182:185], v[108:111]
	v_mfma_f32_16x16x32_bf16 v[92:95], v[104:107], v[190:193], v[92:95]
	v_mfma_f32_16x16x32_bf16 v[88:91], v[136:139], v[190:193], v[88:91]
	v_mfma_f32_16x16x32_bf16 v[76:79], v[104:107], v[204:207], v[76:79]
	v_mfma_f32_16x16x32_bf16 v[72:75], v[136:139], v[204:207], v[72:75]
	v_mfma_f32_16x16x32_bf16 v[132:135], v[124:127], v[178:181], v[132:135]
	v_mfma_f32_16x16x32_bf16 v[128:131], v[140:143], v[178:181], v[128:131]
	v_mfma_f32_16x16x32_bf16 v[112:115], v[124:127], v[186:189], v[112:115]
	v_mfma_f32_16x16x32_bf16 v[108:111], v[140:143], v[186:189], v[108:111]
	v_mfma_f32_16x16x32_bf16 v[92:95], v[124:127], v[194:197], v[92:95]
	v_mfma_f32_16x16x32_bf16 v[88:91], v[140:143], v[194:197], v[88:91]
	v_mfma_f32_16x16x32_bf16 v[76:79], v[124:127], v[208:211], v[76:79]
	v_mfma_f32_16x16x32_bf16 v[72:75], v[140:143], v[208:211], v[72:75]
	s_setprio 0
	s_setprio 1
	v_mfma_f32_16x16x32_bf16 v[120:123], v[144:147], v[174:177], v[120:123]
	v_mfma_f32_16x16x32_bf16 v[116:119], v[152:155], v[174:177], v[116:119]
	v_mfma_f32_16x16x32_bf16 v[100:103], v[144:147], v[182:185], v[100:103]
	v_mfma_f32_16x16x32_bf16 v[96:99], v[152:155], v[182:185], v[96:99]
	v_mfma_f32_16x16x32_bf16 v[84:87], v[144:147], v[190:193], v[84:87]
	v_mfma_f32_16x16x32_bf16 v[80:83], v[152:155], v[190:193], v[80:83]
	v_mfma_f32_16x16x32_bf16 v[68:71], v[144:147], v[204:207], v[68:71]
	v_mfma_f32_16x16x32_bf16 v[64:67], v[152:155], v[204:207], v[64:67]
	v_mfma_f32_16x16x32_bf16 v[120:123], v[148:151], v[178:181], v[120:123]
	v_mfma_f32_16x16x32_bf16 v[116:119], v[156:159], v[178:181], v[116:119]
	v_mfma_f32_16x16x32_bf16 v[100:103], v[148:151], v[186:189], v[100:103]
	v_mfma_f32_16x16x32_bf16 v[96:99], v[156:159], v[186:189], v[96:99]
	v_mfma_f32_16x16x32_bf16 v[84:87], v[148:151], v[194:197], v[84:87]
	v_mfma_f32_16x16x32_bf16 v[80:83], v[156:159], v[194:197], v[80:83]
	v_mfma_f32_16x16x32_bf16 v[68:71], v[148:151], v[208:211], v[68:71]
	v_mfma_f32_16x16x32_bf16 v[64:67], v[156:159], v[208:211], v[64:67]
	s_setprio 0
	s_barrier
	s_add_i32 s87, s74, s33
	s_add_u32 s98, s46, 0x80
	s_addc_u32 s99, s47, 0
	s_mov_b32 m0, s87
	ds_read_b128 v[174:177], v202 offset:16384
	ds_read_b128 v[178:181], v202 offset:17408
	ds_read_b128 v[182:185], v202 offset:18432
	ds_read_b128 v[186:189], v202 offset:19456
	ds_read_b128 v[190:193], v202 offset:20480
	ds_read_b128 v[194:197], v202 offset:21504
	ds_read_b128 v[204:207], v202 offset:22528
	ds_read_b128 v[208:211], v202 offset:23552
	global_load_lds_dwordx4 v162, s[46:47]
	s_add_i32 m0, s87, 0x2000
	s_add_u32 s88, s46, 0x10000
	s_addc_u32 s89, s47, 0
	s_add_i32 s87, s75, s33
	global_load_lds_dwordx4 v166, s[46:47]
	s_mov_b32 m0, s87
	s_add_u32 s100, s44, 0x80
	s_addc_u32 s101, s45, 0
	global_load_lds_dwordx4 v162, s[88:89]
	s_add_i32 m0, s87, 0x2000
	s_nop 0
	global_load_lds_dwordx4 v166, s[88:89]
	s_mov_b32 m0, s60
	s_nop 0
	global_load_lds_dwordx4 v160, s[44:45]
	s_mov_b32 m0, s61
	s_nop 0
	global_load_lds_dwordx4 v164, s[44:45]
	s_cmp_lg_u32 s85, 0
	s_cbranch_scc1 .Lwvr4
	s_waitcnt vmcnt(8)
.Lwvr4:
	s_waitcnt vmcnt(24)
	s_waitcnt lgkmcnt(0)
	s_barrier
	s_setprio 1
	s_waitcnt lgkmcnt(0)
	v_mfma_f32_16x16x32_bf16 v[60:63], v[104:107], v[174:177], v[60:63]
	v_mfma_f32_16x16x32_bf16 v[56:59], v[136:139], v[174:177], v[56:59]
	v_mfma_f32_16x16x32_bf16 v[44:47], v[104:107], v[182:185], v[44:47]
	v_mfma_f32_16x16x32_bf16 v[40:43], v[136:139], v[182:185], v[40:43]
	v_mfma_f32_16x16x32_bf16 v[28:31], v[104:107], v[190:193], v[28:31]
	v_mfma_f32_16x16x32_bf16 v[24:27], v[136:139], v[190:193], v[24:27]
	v_mfma_f32_16x16x32_bf16 v[12:15], v[104:107], v[204:207], v[12:15]
	v_mfma_f32_16x16x32_bf16 v[8:11], v[136:139], v[204:207], v[8:11]
	v_mfma_f32_16x16x32_bf16 v[60:63], v[124:127], v[178:181], v[60:63]
	v_mfma_f32_16x16x32_bf16 v[56:59], v[140:143], v[178:181], v[56:59]
	v_mfma_f32_16x16x32_bf16 v[44:47], v[124:127], v[186:189], v[44:47]
	v_mfma_f32_16x16x32_bf16 v[40:43], v[140:143], v[186:189], v[40:43]
	v_mfma_f32_16x16x32_bf16 v[28:31], v[124:127], v[194:197], v[28:31]
	v_mfma_f32_16x16x32_bf16 v[24:27], v[140:143], v[194:197], v[24:27]
	v_mfma_f32_16x16x32_bf16 v[12:15], v[124:127], v[208:211], v[12:15]
	v_mfma_f32_16x16x32_bf16 v[8:11], v[140:143], v[208:211], v[8:11]
	s_setprio 0
	s_setprio 1
	v_mfma_f32_16x16x32_bf16 v[52:55], v[144:147], v[174:177], v[52:55]
	v_mfma_f32_16x16x32_bf16 v[48:51], v[152:155], v[174:177], v[48:51]
	v_mfma_f32_16x16x32_bf16 v[36:39], v[144:147], v[182:185], v[36:39]
	v_mfma_f32_16x16x32_bf16 v[32:35], v[152:155], v[182:185], v[32:35]
	v_mfma_f32_16x16x32_bf16 v[20:23], v[144:147], v[190:193], v[20:23]
	v_mfma_f32_16x16x32_bf16 v[16:19], v[152:155], v[190:193], v[16:19]
	v_mfma_f32_16x16x32_bf16 v[4:7], v[144:147], v[204:207], v[4:7]
	v_mfma_f32_16x16x32_bf16 v[0:3], v[152:155], v[204:207], v[0:3]
	v_mfma_f32_16x16x32_bf16 v[52:55], v[148:151], v[178:181], v[52:55]
	v_mfma_f32_16x16x32_bf16 v[48:51], v[156:159], v[178:181], v[48:51]
	v_mfma_f32_16x16x32_bf16 v[36:39], v[148:151], v[186:189], v[36:39]
	v_mfma_f32_16x16x32_bf16 v[32:35], v[156:159], v[186:189], v[32:35]
	v_mfma_f32_16x16x32_bf16 v[20:23], v[148:151], v[194:197], v[20:23]
	v_mfma_f32_16x16x32_bf16 v[16:19], v[156:159], v[194:197], v[16:19]
	v_mfma_f32_16x16x32_bf16 v[4:7], v[148:151], v[208:211], v[4:7]
	v_mfma_f32_16x16x32_bf16 v[0:3], v[156:159], v[208:211], v[0:3]
	s_setprio 0
	s_barrier
	s_add_i32 s87, 0, 0x18000
	s_add_i32 s90, 0, 0x1c000
	v_add_u32_e32 v140, s87, v198
	v_add_u32_e32 v156, s90, v198
	ds_read_b128 v[104:107], v140
	ds_read_b128 v[124:127], v140 offset:1024
	ds_read_b128 v[136:139], v140 offset:2048
	ds_read_b128 v[140:143], v140 offset:3072
	ds_read_b128 v[144:147], v156
	ds_read_b128 v[148:151], v156 offset:1024
	ds_read_b128 v[152:155], v156 offset:2048
	ds_read_b128 v[156:159], v156 offset:3072
	s_add_u32 s88, s44, 0x10000
	s_addc_u32 s89, s45, 0
	s_mov_b32 m0, s63
	ds_read_b128 v[174:177], v202 offset:32768
	ds_read_b128 v[178:181], v202 offset:33792
	ds_read_b128 v[182:185], v202 offset:34816
	ds_read_b128 v[186:189], v202 offset:35840
	ds_read_b128 v[190:193], v202 offset:36864
	ds_read_b128 v[194:197], v202 offset:37888
	ds_read_b128 v[204:207], v202 offset:38912
	ds_read_b128 v[208:211], v202 offset:39936
	global_load_lds_dwordx4 v160, s[88:89]
	s_mov_b32 m0, s64
	s_nop 0
	global_load_lds_dwordx4 v164, s[88:89]
	s_cmp_lg_u32 s85, 0
	s_cbranch_scc1 .Lwvr5
	s_waitcnt vmcnt(8)
; #define PG8_STAGE(bufoff, gbase, voff) do { _Pragma("unroll") for (int _i = 0; _i < 2; ++_i) \
;         __builtin_amdgcn_global_load_lds((const unsigned*)((const char*)(gbase) + (voff)[_i]), (LAS unsigned*)(lds + (bufoff) + ldsw + _i * 8192), 16, 0, 0); } while (0)
; #define PG8_LDA(dst, b, h) do { _Pragma("unroll") for (int m = 0; m < 4; ++m) _Pragma("unroll") for (int k = 0; k < 2; ++k) dst[m][k] = *(const LAS bf16x8*)(lds + PG8_SA(b, h) + aoff + m * 2048 + k * 1024); } while (0)
; #define PG8_MMA(ai, bj, At, Bt_) do { __builtin_amdgcn_s_setprio(1); _Pragma("unroll") for (int m = 0; m < 4; ++m) _Pragma("unroll") for (int n = 0; n < 2; ++n) _Pragma("unroll") for (int k = 0; k < 2; ++k) \
;         acc[ai][bj][m][n] = __builtin_amdgcn_mfma_f32_16x16x32_bf16(Bt_[n][k], At[m][k], acc[ai][bj][m][n], 0, 0, 0); __builtin_amdgcn_s_setprio(0); } while (0)
; #define PG8_WAIT_V(n) asm volatile("s_waitcnt vmcnt(" #n ")" ::: "memory")
; #define PG8_WAIT_L(n) asm volatile("s_waitcnt lgkmcnt(" #n ")" ::: "memory")
; #define PG8_WAIT_VR(rl) asm volatile("s_cmp_lg_u32 %0, 0\n\ts_cbranch_scc1 .Lwvr%=\n\ts_waitcnt vmcnt(8)\n.Lwvr%=:\n\ts_waitcnt vmcnt(24)" :: "s"(rl) : "scc", "memory")
; #define PG8_BAR __builtin_amdgcn_s_barrier()
; #define PG8_SCHED __builtin_amdgcn_sched_barrier(0)
; #define PG8_STAGE_A(bufoff, ptr_dense, half, ktoff, goffs) do { if constexpr (GATHER) { PG8_STAGE(bufoff, (const char*)A + (ktoff), goffs); } \
;         else { PG8_STAGE(bufoff, (ptr_dense) + (half) * hstepA, voffA); } } while (0)
; template <class Epi, class Sched, bool GATHER>
; __device__ __forceinline__ void gemm_phase(LAS unsigned char* lds, const int wid, const bf16_t* A, int lda, const bf16_t* Bt, int ldb, size_t b_estride, int K, const Sched& S, const Epi& E) {
;     ...
;             PG8_WAIT_VR(rl); PG8_WAIT_L(0); PG8_BAR; PG8_MMA(0, 0, At, B0); PG8_MMA(0, 1, At, B1); PG8_BAR; PG8_SCHED;
;             PG8_LDA(At, 1, 1); PG8_STAGE(PG8_SB(1, 0), b3, voffB); PG8_STAGE(PG8_SB(1, 1), b3 + hstepB, voffB); PG8_STAGE_A(PG8_SA(1, 0), a3, 0, k3, g20);
;             PG8_WAIT_V(8); PG8_WAIT_L(0); PG8_BAR; PG8_MMA(1, 0, At, B0); PG8_MMA(1, 1, At, B1); PG8_BAR; PG8_SCHED;
;             PG8_STAGE_A(PG8_SA(1, 1), a3, 1, k3, g21);
;         }
.Lwvr5:
	s_waitcnt vmcnt(24)
	s_waitcnt lgkmcnt(0)
	s_barrier
	s_setprio 1
	s_waitcnt lgkmcnt(0)
	v_mfma_f32_16x16x32_bf16 v[132:135], v[104:107], v[174:177], v[132:135]
	v_mfma_f32_16x16x32_bf16 v[128:131], v[136:139], v[174:177], v[128:131]
	v_mfma_f32_16x16x32_bf16 v[112:115], v[104:107], v[182:185], v[112:115]
	v_mfma_f32_16x16x32_bf16 v[108:111], v[136:139], v[182:185], v[108:111]
	v_mfma_f32_16x16x32_bf16 v[92:95], v[104:107], v[190:193], v[92:95]
	v_mfma_f32_16x16x32_bf16 v[88:91], v[136:139], v[190:193], v[88:91]
	v_mfma_f32_16x16x32_bf16 v[76:79], v[104:107], v[204:207], v[76:79]
	v_mfma_f32_16x16x32_bf16 v[72:75], v[136:139], v[204:207], v[72:75]
	v_mfma_f32_16x16x32_bf16 v[132:135], v[124:127], v[178:181], v[132:135]
	v_mfma_f32_16x16x32_bf16 v[128:131], v[140:143], v[178:181], v[128:131]
	v_mfma_f32_16x16x32_bf16 v[112:115], v[124:127], v[186:189], v[112:115]
	v_mfma_f32_16x16x32_bf16 v[108:111], v[140:143], v[186:189], v[108:111]
	v_mfma_f32_16x16x32_bf16 v[92:95], v[124:127], v[194:197], v[92:95]
	v_mfma_f32_16x16x32_bf16 v[88:91], v[140:143], v[194:197], v[88:91]
	v_mfma_f32_16x16x32_bf16 v[76:79], v[124:127], v[208:211], v[76:79]
	v_mfma_f32_16x16x32_bf16 v[72:75], v[140:143], v[208:211], v[72:75]
	s_setprio 0
	s_setprio 1
	v_mfma_f32_16x16x32_bf16 v[120:123], v[144:147], v[174:177], v[120:123]
	v_mfma_f32_16x16x32_bf16 v[116:119], v[152:155], v[174:177], v[116:119]
	v_mfma_f32_16x16x32_bf16 v[100:103], v[144:147], v[182:185], v[100:103]
	v_mfma_f32_16x16x32_bf16 v[96:99], v[152:155], v[182:185], v[96:99]
	v_mfma_f32_16x16x32_bf16 v[84:87], v[144:147], v[190:193], v[84:87]
	v_mfma_f32_16x16x32_bf16 v[80:83], v[152:155], v[190:193], v[80:83]
	v_mfma_f32_16x16x32_bf16 v[68:71], v[144:147], v[204:207], v[68:71]
	v_mfma_f32_16x16x32_bf16 v[64:67], v[152:155], v[204:207], v[64:67]
	v_mfma_f32_16x16x32_bf16 v[120:123], v[148:151], v[178:181], v[120:123]
	v_mfma_f32_16x16x32_bf16 v[116:119], v[156:159], v[178:181], v[116:119]
	v_mfma_f32_16x16x32_bf16 v[100:103], v[148:151], v[186:189], v[100:103]
	v_mfma_f32_16x16x32_bf16 v[96:99], v[156:159], v[186:189], v[96:99]
	v_mfma_f32_16x16x32_bf16 v[84:87], v[148:151], v[194:197], v[84:87]
	v_mfma_f32_16x16x32_bf16 v[80:83], v[156:159], v[194:197], v[80:83]
	v_mfma_f32_16x16x32_bf16 v[68:71], v[148:151], v[208:211], v[68:71]
	v_mfma_f32_16x16x32_bf16 v[64:67], v[156:159], v[208:211], v[64:67]
	s_setprio 0
	s_barrier
	s_add_i32 s85, s87, s33
	s_mov_b32 m0, s85
	ds_read_b128 v[174:177], v202 offset:49152
	ds_read_b128 v[178:181], v202 offset:50176
	ds_read_b128 v[182:185], v202 offset:51200
	ds_read_b128 v[186:189], v202 offset:52224
	ds_read_b128 v[190:193], v202 offset:53248
	ds_read_b128 v[194:197], v202 offset:54272
	ds_read_b128 v[204:207], v202 offset:55296
	ds_read_b128 v[208:211], v202 offset:56320
	global_load_lds_dwordx4 v162, s[98:99]
	s_add_i32 m0, s85, 0x2000
	s_add_u32 s46, s46, 0x10080
	s_addc_u32 s47, s47, 0
	s_add_i32 s85, s90, s33
	global_load_lds_dwordx4 v166, s[98:99]
	s_mov_b32 m0, s85
	s_nop 0
	global_load_lds_dwordx4 v162, s[46:47]
	s_add_i32 m0, s85, 0x2000
	s_nop 0
	global_load_lds_dwordx4 v166, s[46:47]
	s_mov_b32 m0, s66
	s_nop 0
	global_load_lds_dwordx4 v160, s[100:101]
	s_mov_b32 m0, s67
	s_nop 0
	global_load_lds_dwordx4 v164, s[100:101]
	s_waitcnt vmcnt(8)
	s_waitcnt lgkmcnt(0)
	s_barrier
	s_setprio 1
	s_waitcnt lgkmcnt(0)
	v_mfma_f32_16x16x32_bf16 v[60:63], v[104:107], v[174:177], v[60:63]
	v_mfma_f32_16x16x32_bf16 v[56:59], v[136:139], v[174:177], v[56:59]
	v_mfma_f32_16x16x32_bf16 v[44:47], v[104:107], v[182:185], v[44:47]
	v_mfma_f32_16x16x32_bf16 v[40:43], v[136:139], v[182:185], v[40:43]
	v_mfma_f32_16x16x32_bf16 v[28:31], v[104:107], v[190:193], v[28:31]
	v_mfma_f32_16x16x32_bf16 v[24:27], v[136:139], v[190:193], v[24:27]
	v_mfma_f32_16x16x32_bf16 v[12:15], v[104:107], v[204:207], v[12:15]
	v_mfma_f32_16x16x32_bf16 v[8:11], v[136:139], v[204:207], v[8:11]
	v_mfma_f32_16x16x32_bf16 v[60:63], v[124:127], v[178:181], v[60:63]
	v_mfma_f32_16x16x32_bf16 v[56:59], v[140:143], v[178:181], v[56:59]
	v_mfma_f32_16x16x32_bf16 v[44:47], v[124:127], v[186:189], v[44:47]
	v_mfma_f32_16x16x32_bf16 v[40:43], v[140:143], v[186:189], v[40:43]
	v_mfma_f32_16x16x32_bf16 v[28:31], v[124:127], v[194:197], v[28:31]
	v_mfma_f32_16x16x32_bf16 v[24:27], v[140:143], v[194:197], v[24:27]
	v_mfma_f32_16x16x32_bf16 v[12:15], v[124:127], v[208:211], v[12:15]
	v_mfma_f32_16x16x32_bf16 v[8:11], v[140:143], v[208:211], v[8:11]
	s_setprio 0
	s_setprio 1
	v_mfma_f32_16x16x32_bf16 v[52:55], v[144:147], v[174:177], v[52:55]
	v_mfma_f32_16x16x32_bf16 v[48:51], v[152:155], v[174:177], v[48:51]
	v_mfma_f32_16x16x32_bf16 v[36:39], v[144:147], v[182:185], v[36:39]
	v_mfma_f32_16x16x32_bf16 v[32:35], v[152:155], v[182:185], v[32:35]
	v_mfma_f32_16x16x32_bf16 v[20:23], v[144:147], v[190:193], v[20:23]
	v_mfma_f32_16x16x32_bf16 v[16:19], v[152:155], v[190:193], v[16:19]
	v_mfma_f32_16x16x32_bf16 v[4:7], v[144:147], v[204:207], v[4:7]
	v_mfma_f32_16x16x32_bf16 v[0:3], v[152:155], v[204:207], v[0:3]
	v_mfma_f32_16x16x32_bf16 v[52:55], v[148:151], v[178:181], v[52:55]
	v_mfma_f32_16x16x32_bf16 v[48:51], v[156:159], v[178:181], v[48:51]
	v_mfma_f32_16x16x32_bf16 v[36:39], v[148:151], v[186:189], v[36:39]
	v_mfma_f32_16x16x32_bf16 v[32:35], v[156:159], v[186:189], v[32:35]
	v_mfma_f32_16x16x32_bf16 v[20:23], v[148:151], v[194:197], v[20:23]
	v_mfma_f32_16x16x32_bf16 v[16:19], v[156:159], v[194:197], v[16:19]
	v_mfma_f32_16x16x32_bf16 v[4:7], v[148:151], v[208:211], v[4:7]
	v_mfma_f32_16x16x32_bf16 v[0:3], v[156:159], v[208:211], v[0:3]
	s_setprio 0
	s_barrier
	s_add_u32 s44, s44, 0x10080
	s_addc_u32 s45, s45, 0
	s_mov_b32 m0, s68
	s_nop 0
	global_load_lds_dwordx4 v160, s[44:45]
	s_mov_b32 m0, s69
	s_add_u32 s81, s81, 0x100
	global_load_lds_dwordx4 v164, s[44:45]
	s_addc_u32 s82, s82, 0
	s_add_u32 s83, s83, 0x100
	s_addc_u32 s84, s84, 0
	s_cmp_ge_i32 s86, s4
	s_mov_b32 s85, s86
	s_cbranch_scc0 .LBB0_432

; #define PG8_STAGE(bufoff, gbase, voff) do { _Pragma("unroll") for (int _i = 0; _i < 2; ++_i) \
;         __builtin_amdgcn_global_load_lds((const unsigned*)((const char*)(gbase) + (voff)[_i]), (LAS unsigned*)(lds + (bufoff) + ldsw + _i * 8192), 16, 0, 0); } while (0)
; #define PG8_LDA(dst, b, h) do { _Pragma("unroll") for (int m = 0; m < 4; ++m) _Pragma("unroll") for (int k = 0; k < 2; ++k) dst[m][k] = *(const LAS bf16x8*)(lds + PG8_SA(b, h) + aoff + m * 2048 + k * 1024); } while (0)
; #define PG8_LDB(dst, b, h) do { _Pragma("unroll") for (int n = 0; n < 2; ++n) _Pragma("unroll") for (int k = 0; k < 2; ++k) dst[n][k] = *(const LAS bf16x8*)(lds + PG8_SB(b, h) + boff + n * 2048 + k * 1024); } while (0)
; #define PG8_MMA(ai, bj, At, Bt_) do { __builtin_amdgcn_s_setprio(1); _Pragma("unroll") for (int m = 0; m < 4; ++m) _Pragma("unroll") for (int n = 0; n < 2; ++n) _Pragma("unroll") for (int k = 0; k < 2; ++k) \
;         acc[ai][bj][m][n] = __builtin_amdgcn_mfma_f32_16x16x32_bf16(Bt_[n][k], At[m][k], acc[ai][bj][m][n], 0, 0, 0); __builtin_amdgcn_s_setprio(0); } while (0)
; #define PG8_WAIT_L(n) asm volatile("s_waitcnt lgkmcnt(" #n ")" ::: "memory")
; #define PG8_WAIT_VR(rl) asm volatile("s_cmp_lg_u32 %0, 0\n\ts_cbranch_scc1 .Lwvr%=\n\ts_waitcnt vmcnt(8)\n.Lwvr%=:\n\ts_waitcnt vmcnt(24)" :: "s"(rl) : "scc", "memory")
; #define PG8_BAR __builtin_amdgcn_s_barrier()
; #define PG8_SCHED __builtin_amdgcn_sched_barrier(0)
; template <class Epi, class Sched, bool GATHER>
; __device__ __forceinline__ void gemm_phase(LAS unsigned char* lds, const int wid, const bf16_t* A, int lda, const bf16_t* Bt, int ldb, size_t b_estride, int K, const Sched& S, const Epi& E) {
;     ...
;             PG8_WAIT_VR(rl); PG8_WAIT_L(0); PG8_BAR; PG8_MMA(0, 0, At, B0); PG8_MMA(0, 1, At, B1); PG8_BAR; PG8_SCHED;
;             PG8_LDA(At, 0, 1); PG8_STAGE(PG8_SB(0, 0), b2, voffB); PG8_STAGE(PG8_SB(0, 1), b2 + hstepB, voffB); PG8_STAGE_A(PG8_SA(0, 0), a2, 0, k2, g20);
;             PG8_WAIT_VR(rl); PG8_WAIT_L(0); PG8_BAR; PG8_MMA(1, 0, At, B0); PG8_MMA(1, 1, At, B1); PG8_BAR; PG8_SCHED;
;             PG8_LDB(B0, 1, 0); PG8_LDB(B1, 1, 1); PG8_SCHED; PG8_LDA(At, 1, 0); PG8_STAGE_A(PG8_SA(0, 1), a2, 1, k2, g21);
.Lwvr6:
	s_waitcnt vmcnt(24)
	s_waitcnt lgkmcnt(0)
	s_barrier
	s_setprio 1
	s_waitcnt lgkmcnt(0)
	v_mfma_f32_16x16x32_bf16 v[124:127], v[142:145], v[180:183], v[124:127]
	v_mfma_f32_16x16x32_bf16 v[120:123], v[156:159], v[180:183], v[120:123]
	v_mfma_f32_16x16x32_bf16 v[108:111], v[142:145], v[188:191], v[108:111]
	v_mfma_f32_16x16x32_bf16 v[104:107], v[156:159], v[188:191], v[104:107]
	v_mfma_f32_16x16x32_bf16 v[92:95], v[142:145], v[200:203], v[92:95]
	v_mfma_f32_16x16x32_bf16 v[88:91], v[156:159], v[200:203], v[88:91]
	v_mfma_f32_16x16x32_bf16 v[76:79], v[142:145], v[208:211], v[76:79]
	v_mfma_f32_16x16x32_bf16 v[72:75], v[156:159], v[208:211], v[72:75]
	v_mfma_f32_16x16x32_bf16 v[124:127], v[152:155], v[184:187], v[124:127]
	v_mfma_f32_16x16x32_bf16 v[120:123], v[160:163], v[184:187], v[120:123]
	v_mfma_f32_16x16x32_bf16 v[108:111], v[152:155], v[192:195], v[108:111]
	v_mfma_f32_16x16x32_bf16 v[104:107], v[160:163], v[192:195], v[104:107]
	v_mfma_f32_16x16x32_bf16 v[92:95], v[152:155], v[204:207], v[92:95]
	v_mfma_f32_16x16x32_bf16 v[88:91], v[160:163], v[204:207], v[88:91]
	v_mfma_f32_16x16x32_bf16 v[76:79], v[152:155], v[212:215], v[76:79]
	v_mfma_f32_16x16x32_bf16 v[72:75], v[160:163], v[212:215], v[72:75]
	s_setprio 0
	s_setprio 1
	v_mfma_f32_16x16x32_bf16 v[116:119], v[164:167], v[180:183], v[116:119]
	v_mfma_f32_16x16x32_bf16 v[112:115], v[172:175], v[180:183], v[112:115]
	v_mfma_f32_16x16x32_bf16 v[100:103], v[164:167], v[188:191], v[100:103]
	v_mfma_f32_16x16x32_bf16 v[96:99], v[172:175], v[188:191], v[96:99]
	v_mfma_f32_16x16x32_bf16 v[84:87], v[164:167], v[200:203], v[84:87]
	v_mfma_f32_16x16x32_bf16 v[80:83], v[172:175], v[200:203], v[80:83]
	v_mfma_f32_16x16x32_bf16 v[68:71], v[164:167], v[208:211], v[68:71]
	v_mfma_f32_16x16x32_bf16 v[64:67], v[172:175], v[208:211], v[64:67]
	v_mfma_f32_16x16x32_bf16 v[116:119], v[168:171], v[184:187], v[116:119]
	v_mfma_f32_16x16x32_bf16 v[112:115], v[176:179], v[184:187], v[112:115]
	v_mfma_f32_16x16x32_bf16 v[100:103], v[168:171], v[192:195], v[100:103]
	v_mfma_f32_16x16x32_bf16 v[96:99], v[176:179], v[192:195], v[96:99]
	v_mfma_f32_16x16x32_bf16 v[84:87], v[168:171], v[204:207], v[84:87]
	v_mfma_f32_16x16x32_bf16 v[80:83], v[176:179], v[204:207], v[80:83]
	v_mfma_f32_16x16x32_bf16 v[68:71], v[168:171], v[212:215], v[68:71]
	v_mfma_f32_16x16x32_bf16 v[64:67], v[176:179], v[212:215], v[64:67]
	s_setprio 0
	s_barrier
	s_add_i32 s84, s66, s33
	s_add_u32 s98, s42, 0x80
	s_addc_u32 s99, s43, 0
	s_mov_b32 m0, s84
	ds_read_b128 v[180:183], v151 offset:16384
	ds_read_b128 v[184:187], v151 offset:17408
	ds_read_b128 v[188:191], v151 offset:18432
	ds_read_b128 v[192:195], v151 offset:19456
	ds_read_b128 v[200:203], v151 offset:20480
	ds_read_b128 v[204:207], v151 offset:21504
	ds_read_b128 v[208:211], v151 offset:22528
	ds_read_b128 v[212:215], v151 offset:23552
	global_load_lds_dwordx4 v132, s[42:43]
	s_add_i32 m0, s84, 0x2000
	s_add_u32 s84, s42, 0x10000
	s_addc_u32 s85, s43, 0
	s_add_i32 s86, s67, s33
	global_load_lds_dwordx4 v128, s[42:43]
	s_mov_b32 m0, s86
	s_add_u32 s100, s38, 0x80
	s_addc_u32 s101, s39, 0
	global_load_lds_dwordx4 v132, s[84:85]
	s_add_i32 m0, s86, 0x2000
	s_nop 0
	global_load_lds_dwordx4 v128, s[84:85]
	s_mov_b32 m0, s52
	s_nop 0
	global_load_lds_dwordx4 v134, s[38:39]
	s_mov_b32 m0, s53
	s_nop 0
	global_load_lds_dwordx4 v130, s[38:39]
	s_cmp_lg_u32 s82, 0
	s_cbranch_scc1 .Lwvr7
	s_waitcnt vmcnt(8)
.Lwvr7:
	s_waitcnt vmcnt(24)
	s_waitcnt lgkmcnt(0)
	s_barrier
	s_setprio 1
	s_waitcnt lgkmcnt(0)
	v_mfma_f32_16x16x32_bf16 v[60:63], v[142:145], v[180:183], v[60:63]
	v_mfma_f32_16x16x32_bf16 v[56:59], v[156:159], v[180:183], v[56:59]
	v_mfma_f32_16x16x32_bf16 v[44:47], v[142:145], v[188:191], v[44:47]
	v_mfma_f32_16x16x32_bf16 v[40:43], v[156:159], v[188:191], v[40:43]
	v_mfma_f32_16x16x32_bf16 v[28:31], v[142:145], v[200:203], v[28:31]
	v_mfma_f32_16x16x32_bf16 v[24:27], v[156:159], v[200:203], v[24:27]
	v_mfma_f32_16x16x32_bf16 v[12:15], v[142:145], v[208:211], v[12:15]
	v_mfma_f32_16x16x32_bf16 v[8:11], v[156:159], v[208:211], v[8:11]
	v_mfma_f32_16x16x32_bf16 v[60:63], v[152:155], v[184:187], v[60:63]
	v_mfma_f32_16x16x32_bf16 v[56:59], v[160:163], v[184:187], v[56:59]
	v_mfma_f32_16x16x32_bf16 v[44:47], v[152:155], v[192:195], v[44:47]
	v_mfma_f32_16x16x32_bf16 v[40:43], v[160:163], v[192:195], v[40:43]
	v_mfma_f32_16x16x32_bf16 v[28:31], v[152:155], v[204:207], v[28:31]
	v_mfma_f32_16x16x32_bf16 v[24:27], v[160:163], v[204:207], v[24:27]
	v_mfma_f32_16x16x32_bf16 v[12:15], v[152:155], v[212:215], v[12:15]
	v_mfma_f32_16x16x32_bf16 v[8:11], v[160:163], v[212:215], v[8:11]
	s_setprio 0
	s_setprio 1
	v_mfma_f32_16x16x32_bf16 v[52:55], v[164:167], v[180:183], v[52:55]
	v_mfma_f32_16x16x32_bf16 v[48:51], v[172:175], v[180:183], v[48:51]
	v_mfma_f32_16x16x32_bf16 v[36:39], v[164:167], v[188:191], v[36:39]
	v_mfma_f32_16x16x32_bf16 v[32:35], v[172:175], v[188:191], v[32:35]
	v_mfma_f32_16x16x32_bf16 v[20:23], v[164:167], v[200:203], v[20:23]
	v_mfma_f32_16x16x32_bf16 v[16:19], v[172:175], v[200:203], v[16:19]
	v_mfma_f32_16x16x32_bf16 v[4:7], v[164:167], v[208:211], v[4:7]
	v_mfma_f32_16x16x32_bf16 v[0:3], v[172:175], v[208:211], v[0:3]
	v_mfma_f32_16x16x32_bf16 v[52:55], v[168:171], v[184:187], v[52:55]
	v_mfma_f32_16x16x32_bf16 v[48:51], v[176:179], v[184:187], v[48:51]
	v_mfma_f32_16x16x32_bf16 v[36:39], v[168:171], v[192:195], v[36:39]
	v_mfma_f32_16x16x32_bf16 v[32:35], v[176:179], v[192:195], v[32:35]
	v_mfma_f32_16x16x32_bf16 v[20:23], v[168:171], v[204:207], v[20:23]
	v_mfma_f32_16x16x32_bf16 v[16:19], v[176:179], v[204:207], v[16:19]
	v_mfma_f32_16x16x32_bf16 v[4:7], v[168:171], v[212:215], v[4:7]
	v_mfma_f32_16x16x32_bf16 v[0:3], v[176:179], v[212:215], v[0:3]
	s_setprio 0
	s_barrier
	s_add_i32 s86, 0, 0x18000
	v_add_u32_e32 v140, s86, v141
	s_add_i32 s87, 0, 0x1c000
	ds_read_b128 v[142:145], v140
	ds_read_b128 v[152:155], v140 offset:1024
	ds_read_b128 v[156:159], v140 offset:2048
	ds_read_b128 v[160:163], v140 offset:3072
	v_add_u32_e32 v140, s87, v141
	ds_read_b128 v[164:167], v140
	ds_read_b128 v[168:171], v140 offset:1024
	ds_read_b128 v[172:175], v140 offset:2048
	ds_read_b128 v[176:179], v140 offset:3072
	s_add_u32 s84, s38, 0x10000
	s_addc_u32 s85, s39, 0
	s_mov_b32 m0, s58
	ds_read_b128 v[180:183], v151 offset:32768
	ds_read_b128 v[184:187], v151 offset:33792
	ds_read_b128 v[188:191], v151 offset:34816
	ds_read_b128 v[192:195], v151 offset:35840
	ds_read_b128 v[200:203], v151 offset:36864
	ds_read_b128 v[204:207], v151 offset:37888
	ds_read_b128 v[208:211], v151 offset:38912
	ds_read_b128 v[212:215], v151 offset:39936
	global_load_lds_dwordx4 v134, s[84:85]
	s_mov_b32 m0, s59
	s_nop 0
	global_load_lds_dwordx4 v130, s[84:85]
	s_cmp_lg_u32 s82, 0
	s_cbranch_scc1 .Lwvr8
	s_waitcnt vmcnt(8)
; #define PG8_STAGE(bufoff, gbase, voff) do { _Pragma("unroll") for (int _i = 0; _i < 2; ++_i) \
;         __builtin_amdgcn_global_load_lds((const unsigned*)((const char*)(gbase) + (voff)[_i]), (LAS unsigned*)(lds + (bufoff) + ldsw + _i * 8192), 16, 0, 0); } while (0)
; #define PG8_LDA(dst, b, h) do { _Pragma("unroll") for (int m = 0; m < 4; ++m) _Pragma("unroll") for (int k = 0; k < 2; ++k) dst[m][k] = *(const LAS bf16x8*)(lds + PG8_SA(b, h) + aoff + m * 2048 + k * 1024); } while (0)
; #define PG8_MMA(ai, bj, At, Bt_) do { __builtin_amdgcn_s_setprio(1); _Pragma("unroll") for (int m = 0; m < 4; ++m) _Pragma("unroll") for (int n = 0; n < 2; ++n) _Pragma("unroll") for (int k = 0; k < 2; ++k) \
;         acc[ai][bj][m][n] = __builtin_amdgcn_mfma_f32_16x16x32_bf16(Bt_[n][k], At[m][k], acc[ai][bj][m][n], 0, 0, 0); __builtin_amdgcn_s_setprio(0); } while (0)
; #define PG8_WAIT_V(n) asm volatile("s_waitcnt vmcnt(" #n ")" ::: "memory")
; #define PG8_WAIT_L(n) asm volatile("s_waitcnt lgkmcnt(" #n ")" ::: "memory")
; #define PG8_WAIT_VR(rl) asm volatile("s_cmp_lg_u32 %0, 0\n\ts_cbranch_scc1 .Lwvr%=\n\ts_waitcnt vmcnt(8)\n.Lwvr%=:\n\ts_waitcnt vmcnt(24)" :: "s"(rl) : "scc", "memory")
; #define PG8_BAR __builtin_amdgcn_s_barrier()
; #define PG8_SCHED __builtin_amdgcn_sched_barrier(0)
; #define PG8_STAGE_A(bufoff, ptr_dense, half, ktoff, goffs) do { if constexpr (GATHER) { PG8_STAGE(bufoff, (const char*)A + (ktoff), goffs); } \
;         else { PG8_STAGE(bufoff, (ptr_dense) + (half) * hstepA, voffA); } } while (0)
; template <class Epi, class Sched, bool GATHER>
; __device__ __forceinline__ void gemm_phase(LAS unsigned char* lds, const int wid, const bf16_t* A, int lda, const bf16_t* Bt, int ldb, size_t b_estride, int K, const Sched& S, const Epi& E) {
;     ...
;             PG8_WAIT_VR(rl); PG8_WAIT_L(0); PG8_BAR; PG8_MMA(0, 0, At, B0); PG8_MMA(0, 1, At, B1); PG8_BAR; PG8_SCHED;
;             PG8_LDA(At, 1, 1); PG8_STAGE(PG8_SB(1, 0), b3, voffB); PG8_STAGE(PG8_SB(1, 1), b3 + hstepB, voffB); PG8_STAGE_A(PG8_SA(1, 0), a3, 0, k3, g20);
;             PG8_WAIT_V(8); PG8_WAIT_L(0); PG8_BAR; PG8_MMA(1, 0, At, B0); PG8_MMA(1, 1, At, B1); PG8_BAR; PG8_SCHED;
;             PG8_STAGE_A(PG8_SA(1, 1), a3, 1, k3, g21);
;         }
.Lwvr8:
	s_waitcnt vmcnt(24)
	s_waitcnt lgkmcnt(0)
	s_barrier
	s_setprio 1
	s_waitcnt lgkmcnt(0)
	v_mfma_f32_16x16x32_bf16 v[124:127], v[142:145], v[180:183], v[124:127]
	v_mfma_f32_16x16x32_bf16 v[120:123], v[156:159], v[180:183], v[120:123]
	v_mfma_f32_16x16x32_bf16 v[108:111], v[142:145], v[188:191], v[108:111]
	v_mfma_f32_16x16x32_bf16 v[104:107], v[156:159], v[188:191], v[104:107]
	v_mfma_f32_16x16x32_bf16 v[92:95], v[142:145], v[200:203], v[92:95]
	v_mfma_f32_16x16x32_bf16 v[88:91], v[156:159], v[200:203], v[88:91]
	v_mfma_f32_16x16x32_bf16 v[76:79], v[142:145], v[208:211], v[76:79]
	v_mfma_f32_16x16x32_bf16 v[72:75], v[156:159], v[208:211], v[72:75]
	v_mfma_f32_16x16x32_bf16 v[124:127], v[152:155], v[184:187], v[124:127]
	v_mfma_f32_16x16x32_bf16 v[120:123], v[160:163], v[184:187], v[120:123]
	v_mfma_f32_16x16x32_bf16 v[108:111], v[152:155], v[192:195], v[108:111]
	v_mfma_f32_16x16x32_bf16 v[104:107], v[160:163], v[192:195], v[104:107]
	v_mfma_f32_16x16x32_bf16 v[92:95], v[152:155], v[204:207], v[92:95]
	v_mfma_f32_16x16x32_bf16 v[88:91], v[160:163], v[204:207], v[88:91]
	v_mfma_f32_16x16x32_bf16 v[76:79], v[152:155], v[212:215], v[76:79]
	v_mfma_f32_16x16x32_bf16 v[72:75], v[160:163], v[212:215], v[72:75]
	s_setprio 0
	s_setprio 1
	v_mfma_f32_16x16x32_bf16 v[116:119], v[164:167], v[180:183], v[116:119]
	v_mfma_f32_16x16x32_bf16 v[112:115], v[172:175], v[180:183], v[112:115]
	v_mfma_f32_16x16x32_bf16 v[100:103], v[164:167], v[188:191], v[100:103]
	v_mfma_f32_16x16x32_bf16 v[96:99], v[172:175], v[188:191], v[96:99]
	v_mfma_f32_16x16x32_bf16 v[84:87], v[164:167], v[200:203], v[84:87]
	v_mfma_f32_16x16x32_bf16 v[80:83], v[172:175], v[200:203], v[80:83]
	v_mfma_f32_16x16x32_bf16 v[68:71], v[164:167], v[208:211], v[68:71]
	v_mfma_f32_16x16x32_bf16 v[64:67], v[172:175], v[208:211], v[64:67]
	v_mfma_f32_16x16x32_bf16 v[116:119], v[168:171], v[184:187], v[116:119]
	v_mfma_f32_16x16x32_bf16 v[112:115], v[176:179], v[184:187], v[112:115]
	v_mfma_f32_16x16x32_bf16 v[100:103], v[168:171], v[192:195], v[100:103]
	v_mfma_f32_16x16x32_bf16 v[96:99], v[176:179], v[192:195], v[96:99]
	v_mfma_f32_16x16x32_bf16 v[84:87], v[168:171], v[204:207], v[84:87]
	v_mfma_f32_16x16x32_bf16 v[80:83], v[176:179], v[204:207], v[80:83]
	v_mfma_f32_16x16x32_bf16 v[68:71], v[168:171], v[212:215], v[68:71]
	v_mfma_f32_16x16x32_bf16 v[64:67], v[176:179], v[212:215], v[64:67]
	s_setprio 0
	s_barrier
	s_add_i32 s82, s86, s33
	s_mov_b32 m0, s82
	ds_read_b128 v[180:183], v151 offset:49152
	ds_read_b128 v[184:187], v151 offset:50176
	ds_read_b128 v[188:191], v151 offset:51200
	ds_read_b128 v[192:195], v151 offset:52224
	ds_read_b128 v[200:203], v151 offset:53248
	ds_read_b128 v[204:207], v151 offset:54272
	ds_read_b128 v[208:211], v151 offset:55296
	ds_read_b128 v[212:215], v151 offset:56320
	global_load_lds_dwordx4 v132, s[98:99]
	s_add_i32 m0, s82, 0x2000
	s_add_u32 s42, s42, 0x10080
	s_addc_u32 s43, s43, 0
	s_add_i32 s82, s87, s33
	global_load_lds_dwordx4 v128, s[98:99]
	s_mov_b32 m0, s82
	s_nop 0
	global_load_lds_dwordx4 v132, s[42:43]
	s_add_i32 m0, s82, 0x2000
	s_nop 0
	global_load_lds_dwordx4 v128, s[42:43]
	s_mov_b32 m0, s61
	s_nop 0
	global_load_lds_dwordx4 v134, s[100:101]
	s_mov_b32 m0, s63
	s_nop 0
	global_load_lds_dwordx4 v130, s[100:101]
	s_waitcnt vmcnt(8)
	s_waitcnt lgkmcnt(0)
	s_barrier
	s_setprio 1
	s_waitcnt lgkmcnt(0)
	v_mfma_f32_16x16x32_bf16 v[60:63], v[142:145], v[180:183], v[60:63]
	v_mfma_f32_16x16x32_bf16 v[56:59], v[156:159], v[180:183], v[56:59]
	v_mfma_f32_16x16x32_bf16 v[44:47], v[142:145], v[188:191], v[44:47]
	v_mfma_f32_16x16x32_bf16 v[40:43], v[156:159], v[188:191], v[40:43]
	v_mfma_f32_16x16x32_bf16 v[28:31], v[142:145], v[200:203], v[28:31]
	v_mfma_f32_16x16x32_bf16 v[24:27], v[156:159], v[200:203], v[24:27]
	v_mfma_f32_16x16x32_bf16 v[12:15], v[142:145], v[208:211], v[12:15]
	v_mfma_f32_16x16x32_bf16 v[8:11], v[156:159], v[208:211], v[8:11]
	v_mfma_f32_16x16x32_bf16 v[60:63], v[152:155], v[184:187], v[60:63]
	v_mfma_f32_16x16x32_bf16 v[56:59], v[160:163], v[184:187], v[56:59]
	v_mfma_f32_16x16x32_bf16 v[44:47], v[152:155], v[192:195], v[44:47]
	v_mfma_f32_16x16x32_bf16 v[40:43], v[160:163], v[192:195], v[40:43]
	v_mfma_f32_16x16x32_bf16 v[28:31], v[152:155], v[204:207], v[28:31]
	v_mfma_f32_16x16x32_bf16 v[24:27], v[160:163], v[204:207], v[24:27]
	v_mfma_f32_16x16x32_bf16 v[12:15], v[152:155], v[212:215], v[12:15]
	v_mfma_f32_16x16x32_bf16 v[8:11], v[160:163], v[212:215], v[8:11]
	s_setprio 0
	s_setprio 1
	v_mfma_f32_16x16x32_bf16 v[52:55], v[164:167], v[180:183], v[52:55]
	v_mfma_f32_16x16x32_bf16 v[48:51], v[172:175], v[180:183], v[48:51]
	v_mfma_f32_16x16x32_bf16 v[36:39], v[164:167], v[188:191], v[36:39]
	v_mfma_f32_16x16x32_bf16 v[32:35], v[172:175], v[188:191], v[32:35]
	v_mfma_f32_16x16x32_bf16 v[20:23], v[164:167], v[200:203], v[20:23]
	v_mfma_f32_16x16x32_bf16 v[16:19], v[172:175], v[200:203], v[16:19]
	v_mfma_f32_16x16x32_bf16 v[4:7], v[164:167], v[208:211], v[4:7]
	v_mfma_f32_16x16x32_bf16 v[0:3], v[172:175], v[208:211], v[0:3]
	v_mfma_f32_16x16x32_bf16 v[52:55], v[168:171], v[184:187], v[52:55]
	v_mfma_f32_16x16x32_bf16 v[48:51], v[176:179], v[184:187], v[48:51]
	v_mfma_f32_16x16x32_bf16 v[36:39], v[168:171], v[192:195], v[36:39]
	v_mfma_f32_16x16x32_bf16 v[32:35], v[176:179], v[192:195], v[32:35]
	v_mfma_f32_16x16x32_bf16 v[20:23], v[168:171], v[204:207], v[20:23]
	v_mfma_f32_16x16x32_bf16 v[16:19], v[176:179], v[204:207], v[16:19]
	v_mfma_f32_16x16x32_bf16 v[4:7], v[168:171], v[212:215], v[4:7]
	v_mfma_f32_16x16x32_bf16 v[0:3], v[176:179], v[212:215], v[0:3]
	s_setprio 0
	s_barrier
	s_add_u32 s38, s38, 0x10080
	s_addc_u32 s39, s39, 0
	s_mov_b32 m0, s64
	s_nop 0
	global_load_lds_dwordx4 v134, s[38:39]
	s_mov_b32 m0, s65
	s_add_u32 s78, s78, 0x100
	global_load_lds_dwordx4 v130, s[38:39]
	s_addc_u32 s79, s79, 0
	s_add_u32 s80, s80, 0x100
	s_addc_u32 s81, s81, 0
	s_cmp_ge_i32 s83, s4
	s_mov_b32 s82, s83
	s_cbranch_scc0 .LBB0_503

; #define PG8_STAGE(bufoff, gbase, voff) do { _Pragma("unroll") for (int _i = 0; _i < 2; ++_i) \
;         __builtin_amdgcn_global_load_lds((const unsigned*)((const char*)(gbase) + (voff)[_i]), (LAS unsigned*)(lds + (bufoff) + ldsw + _i * 8192), 16, 0, 0); } while (0)
; #define PG8_LDA(dst, b, h) do { _Pragma("unroll") for (int m = 0; m < 4; ++m) _Pragma("unroll") for (int k = 0; k < 2; ++k) dst[m][k] = *(const LAS bf16x8*)(lds + PG8_SA(b, h) + aoff + m * 2048 + k * 1024); } while (0)
; #define PG8_LDB(dst, b, h) do { _Pragma("unroll") for (int n = 0; n < 2; ++n) _Pragma("unroll") for (int k = 0; k < 2; ++k) dst[n][k] = *(const LAS bf16x8*)(lds + PG8_SB(b, h) + boff + n * 2048 + k * 1024); } while (0)
; #define PG8_MMA(ai, bj, At, Bt_) do { __builtin_amdgcn_s_setprio(1); _Pragma("unroll") for (int m = 0; m < 4; ++m) _Pragma("unroll") for (int n = 0; n < 2; ++n) _Pragma("unroll") for (int k = 0; k < 2; ++k) \
;         acc[ai][bj][m][n] = __builtin_amdgcn_mfma_f32_16x16x32_bf16(Bt_[n][k], At[m][k], acc[ai][bj][m][n], 0, 0, 0); __builtin_amdgcn_s_setprio(0); } while (0)
; #define PG8_WAIT_L(n) asm volatile("s_waitcnt lgkmcnt(" #n ")" ::: "memory")
; #define PG8_WAIT_VR(rl) asm volatile("s_cmp_lg_u32 %0, 0\n\ts_cbranch_scc1 .Lwvr%=\n\ts_waitcnt vmcnt(8)\n.Lwvr%=:\n\ts_waitcnt vmcnt(24)" :: "s"(rl) : "scc", "memory")
; #define PG8_BAR __builtin_amdgcn_s_barrier()
; #define PG8_SCHED __builtin_amdgcn_sched_barrier(0)
; template <class Epi, class Sched, bool GATHER>
; __device__ __forceinline__ void gemm_phase(LAS unsigned char* lds, const int wid, const bf16_t* A, int lda, const bf16_t* Bt, int ldb, size_t b_estride, int K, const Sched& S, const Epi& E) {
;     ...
;             PG8_WAIT_VR(rl); PG8_WAIT_L(0); PG8_BAR; PG8_MMA(0, 0, At, B0); PG8_MMA(0, 1, At, B1); PG8_BAR; PG8_SCHED;
;             PG8_LDA(At, 0, 1); PG8_STAGE(PG8_SB(0, 0), b2, voffB); PG8_STAGE(PG8_SB(0, 1), b2 + hstepB, voffB); PG8_STAGE_A(PG8_SA(0, 0), a2, 0, k2, g20);
;             PG8_WAIT_VR(rl); PG8_WAIT_L(0); PG8_BAR; PG8_MMA(1, 0, At, B0); PG8_MMA(1, 1, At, B1); PG8_BAR; PG8_SCHED;
;             PG8_LDB(B0, 1, 0); PG8_LDB(B1, 1, 1); PG8_SCHED; PG8_LDA(At, 1, 0); PG8_STAGE_A(PG8_SA(0, 1), a2, 1, k2, g21);
.Lwvr9:
	s_waitcnt vmcnt(24)
	s_waitcnt lgkmcnt(0)
	s_barrier
	s_setprio 1
	s_waitcnt lgkmcnt(0)
	v_mfma_f32_16x16x32_bf16 v[124:127], v[128:131], v[172:175], v[124:127]
	v_mfma_f32_16x16x32_bf16 v[120:123], v[136:139], v[172:175], v[120:123]
	v_mfma_f32_16x16x32_bf16 v[116:119], v[128:131], v[180:183], v[116:119]
	v_mfma_f32_16x16x32_bf16 v[112:115], v[136:139], v[180:183], v[112:115]
	v_mfma_f32_16x16x32_bf16 v[92:95], v[128:131], v[188:191], v[92:95]
	v_mfma_f32_16x16x32_bf16 v[88:91], v[136:139], v[188:191], v[88:91]
	v_mfma_f32_16x16x32_bf16 v[84:87], v[128:131], v[200:203], v[84:87]
	v_mfma_f32_16x16x32_bf16 v[80:83], v[136:139], v[200:203], v[80:83]
	v_mfma_f32_16x16x32_bf16 v[124:127], v[132:135], v[176:179], v[124:127]
	v_mfma_f32_16x16x32_bf16 v[120:123], v[140:143], v[176:179], v[120:123]
	v_mfma_f32_16x16x32_bf16 v[116:119], v[132:135], v[184:187], v[116:119]
	v_mfma_f32_16x16x32_bf16 v[112:115], v[140:143], v[184:187], v[112:115]
	v_mfma_f32_16x16x32_bf16 v[92:95], v[132:135], v[192:195], v[92:95]
	v_mfma_f32_16x16x32_bf16 v[88:91], v[140:143], v[192:195], v[88:91]
	v_mfma_f32_16x16x32_bf16 v[84:87], v[132:135], v[204:207], v[84:87]
	v_mfma_f32_16x16x32_bf16 v[80:83], v[140:143], v[204:207], v[80:83]
	s_setprio 0
	s_setprio 1
	v_mfma_f32_16x16x32_bf16 v[108:111], v[152:155], v[172:175], v[108:111]
	v_mfma_f32_16x16x32_bf16 v[104:107], v[164:167], v[172:175], v[104:107]
	v_mfma_f32_16x16x32_bf16 v[100:103], v[152:155], v[180:183], v[100:103]
	v_mfma_f32_16x16x32_bf16 v[96:99], v[164:167], v[180:183], v[96:99]
	v_mfma_f32_16x16x32_bf16 v[76:79], v[152:155], v[188:191], v[76:79]
	v_mfma_f32_16x16x32_bf16 v[72:75], v[164:167], v[188:191], v[72:75]
	v_mfma_f32_16x16x32_bf16 v[68:71], v[152:155], v[200:203], v[68:71]
	v_mfma_f32_16x16x32_bf16 v[64:67], v[164:167], v[200:203], v[64:67]
	v_mfma_f32_16x16x32_bf16 v[108:111], v[156:159], v[176:179], v[108:111]
	v_mfma_f32_16x16x32_bf16 v[104:107], v[168:171], v[176:179], v[104:107]
	v_mfma_f32_16x16x32_bf16 v[100:103], v[156:159], v[184:187], v[100:103]
	v_mfma_f32_16x16x32_bf16 v[96:99], v[168:171], v[184:187], v[96:99]
	v_mfma_f32_16x16x32_bf16 v[76:79], v[156:159], v[192:195], v[76:79]
	v_mfma_f32_16x16x32_bf16 v[72:75], v[168:171], v[192:195], v[72:75]
	v_mfma_f32_16x16x32_bf16 v[68:71], v[156:159], v[204:207], v[68:71]
	v_mfma_f32_16x16x32_bf16 v[64:67], v[168:171], v[204:207], v[64:67]
	s_setprio 0
	s_barrier
	s_add_i32 s74, s61, s33
	s_add_u32 s98, s38, 0x80
	s_addc_u32 s99, s39, 0
	s_mov_b32 m0, s74
	ds_read_b128 v[172:175], v163 offset:16384
	ds_read_b128 v[176:179], v163 offset:17408
	ds_read_b128 v[180:183], v163 offset:18432
	ds_read_b128 v[184:187], v163 offset:19456
	ds_read_b128 v[188:191], v163 offset:20480
	ds_read_b128 v[192:195], v163 offset:21504
	ds_read_b128 v[200:203], v163 offset:22528
	ds_read_b128 v[204:207], v163 offset:23552
	global_load_lds_dwordx4 v146, s[38:39]
	s_add_i32 m0, s74, 0x2000
	s_add_u32 s74, s38, 0x40000
	s_addc_u32 s75, s39, 0
	s_add_i32 s77, s63, s33
	global_load_lds_dwordx4 v144, s[38:39]
	s_mov_b32 m0, s77
	s_add_u32 s100, s36, 0x80
	s_addc_u32 s101, s37, 0
	global_load_lds_dwordx4 v146, s[74:75]
	s_add_i32 m0, s77, 0x2000
	s_nop 0
	global_load_lds_dwordx4 v144, s[74:75]
	s_mov_b32 m0, s31
	s_nop 0
	global_load_lds_dwordx4 v146, s[36:37]
	s_mov_b32 m0, s44
	s_nop 0
	global_load_lds_dwordx4 v144, s[36:37]
	s_cmp_lg_u32 s76, 0
	s_cbranch_scc1 .Lwvr10
	s_waitcnt vmcnt(8)

; #define PG8_STAGE(bufoff, gbase, voff) do { _Pragma("unroll") for (int _i = 0; _i < 2; ++_i) \
;         __builtin_amdgcn_global_load_lds((const unsigned*)((const char*)(gbase) + (voff)[_i]), (LAS unsigned*)(lds + (bufoff) + ldsw + _i * 8192), 16, 0, 0); } while (0)
; #define PG8_LDA(dst, b, h) do { _Pragma("unroll") for (int m = 0; m < 4; ++m) _Pragma("unroll") for (int k = 0; k < 2; ++k) dst[m][k] = *(const LAS bf16x8*)(lds + PG8_SA(b, h) + aoff + m * 2048 + k * 1024); } while (0)
; #define PG8_MMA(ai, bj, At, Bt_) do { __builtin_amdgcn_s_setprio(1); _Pragma("unroll") for (int m = 0; m < 4; ++m) _Pragma("unroll") for (int n = 0; n < 2; ++n) _Pragma("unroll") for (int k = 0; k < 2; ++k) \
;         acc[ai][bj][m][n] = __builtin_amdgcn_mfma_f32_16x16x32_bf16(Bt_[n][k], At[m][k], acc[ai][bj][m][n], 0, 0, 0); __builtin_amdgcn_s_setprio(0); } while (0)
; #define PG8_WAIT_V(n) asm volatile("s_waitcnt vmcnt(" #n ")" ::: "memory")
; #define PG8_WAIT_L(n) asm volatile("s_waitcnt lgkmcnt(" #n ")" ::: "memory")
; #define PG8_WAIT_VR(rl) asm volatile("s_cmp_lg_u32 %0, 0\n\ts_cbranch_scc1 .Lwvr%=\n\ts_waitcnt vmcnt(8)\n.Lwvr%=:\n\ts_waitcnt vmcnt(24)" :: "s"(rl) : "scc", "memory")
; #define PG8_BAR __builtin_amdgcn_s_barrier()
; #define PG8_SCHED __builtin_amdgcn_sched_barrier(0)
; #define PG8_STAGE_A(bufoff, ptr_dense, half, ktoff, goffs) do { if constexpr (GATHER) { PG8_STAGE(bufoff, (const char*)A + (ktoff), goffs); } \
;         else { PG8_STAGE(bufoff, (ptr_dense) + (half) * hstepA, voffA); } } while (0)
; template <class Epi, class Sched, bool GATHER>
; __device__ __forceinline__ void gemm_phase(LAS unsigned char* lds, const int wid, const bf16_t* A, int lda, const bf16_t* Bt, int ldb, size_t b_estride, int K, const Sched& S, const Epi& E) {
;     ...
;             PG8_WAIT_VR(rl); PG8_WAIT_L(0); PG8_BAR; PG8_MMA(0, 0, At, B0); PG8_MMA(0, 1, At, B1); PG8_BAR; PG8_SCHED;
;             PG8_LDA(At, 1, 1); PG8_STAGE(PG8_SB(1, 0), b3, voffB); PG8_STAGE(PG8_SB(1, 1), b3 + hstepB, voffB); PG8_STAGE_A(PG8_SA(1, 0), a3, 0, k3, g20);
;             PG8_WAIT_V(8); PG8_WAIT_L(0); PG8_BAR; PG8_MMA(1, 0, At, B0); PG8_MMA(1, 1, At, B1); PG8_BAR; PG8_SCHED;
;             PG8_STAGE_A(PG8_SA(1, 1), a3, 1, k3, g21);
;         }
.Lwvr11:
	s_waitcnt vmcnt(24)
	s_waitcnt lgkmcnt(0)
	s_barrier
	s_setprio 1
	s_waitcnt lgkmcnt(0)
	v_mfma_f32_16x16x32_bf16 v[124:127], v[128:131], v[172:175], v[124:127]
	v_mfma_f32_16x16x32_bf16 v[120:123], v[136:139], v[172:175], v[120:123]
	v_mfma_f32_16x16x32_bf16 v[116:119], v[128:131], v[180:183], v[116:119]
	v_mfma_f32_16x16x32_bf16 v[112:115], v[136:139], v[180:183], v[112:115]
	v_mfma_f32_16x16x32_bf16 v[92:95], v[128:131], v[188:191], v[92:95]
	v_mfma_f32_16x16x32_bf16 v[88:91], v[136:139], v[188:191], v[88:91]
	v_mfma_f32_16x16x32_bf16 v[84:87], v[128:131], v[200:203], v[84:87]
	v_mfma_f32_16x16x32_bf16 v[80:83], v[136:139], v[200:203], v[80:83]
	v_mfma_f32_16x16x32_bf16 v[124:127], v[132:135], v[176:179], v[124:127]
	v_mfma_f32_16x16x32_bf16 v[120:123], v[140:143], v[176:179], v[120:123]
	v_mfma_f32_16x16x32_bf16 v[116:119], v[132:135], v[184:187], v[116:119]
	v_mfma_f32_16x16x32_bf16 v[112:115], v[140:143], v[184:187], v[112:115]
	v_mfma_f32_16x16x32_bf16 v[92:95], v[132:135], v[192:195], v[92:95]
	v_mfma_f32_16x16x32_bf16 v[88:91], v[140:143], v[192:195], v[88:91]
	v_mfma_f32_16x16x32_bf16 v[84:87], v[132:135], v[204:207], v[84:87]
	v_mfma_f32_16x16x32_bf16 v[80:83], v[140:143], v[204:207], v[80:83]
	s_setprio 0
	s_setprio 1
	v_mfma_f32_16x16x32_bf16 v[108:111], v[152:155], v[172:175], v[108:111]
	v_mfma_f32_16x16x32_bf16 v[104:107], v[164:167], v[172:175], v[104:107]
	v_mfma_f32_16x16x32_bf16 v[100:103], v[152:155], v[180:183], v[100:103]
	v_mfma_f32_16x16x32_bf16 v[96:99], v[164:167], v[180:183], v[96:99]
	v_mfma_f32_16x16x32_bf16 v[76:79], v[152:155], v[188:191], v[76:79]
	v_mfma_f32_16x16x32_bf16 v[72:75], v[164:167], v[188:191], v[72:75]
	v_mfma_f32_16x16x32_bf16 v[68:71], v[152:155], v[200:203], v[68:71]
	v_mfma_f32_16x16x32_bf16 v[64:67], v[164:167], v[200:203], v[64:67]
	v_mfma_f32_16x16x32_bf16 v[108:111], v[156:159], v[176:179], v[108:111]
	v_mfma_f32_16x16x32_bf16 v[104:107], v[168:171], v[176:179], v[104:107]
	v_mfma_f32_16x16x32_bf16 v[100:103], v[156:159], v[184:187], v[100:103]
	v_mfma_f32_16x16x32_bf16 v[96:99], v[168:171], v[184:187], v[96:99]
	v_mfma_f32_16x16x32_bf16 v[76:79], v[156:159], v[192:195], v[76:79]
	v_mfma_f32_16x16x32_bf16 v[72:75], v[168:171], v[192:195], v[72:75]
	v_mfma_f32_16x16x32_bf16 v[68:71], v[156:159], v[204:207], v[68:71]
	v_mfma_f32_16x16x32_bf16 v[64:67], v[168:171], v[204:207], v[64:67]
	s_setprio 0
	s_barrier
	s_add_i32 s74, s77, s33
	s_mov_b32 m0, s74
	ds_read_b128 v[172:175], v163 offset:49152
	ds_read_b128 v[176:179], v163 offset:50176
	ds_read_b128 v[180:183], v163 offset:51200
	ds_read_b128 v[184:187], v163 offset:52224
	ds_read_b128 v[188:191], v163 offset:53248
	ds_read_b128 v[192:195], v163 offset:54272
	ds_read_b128 v[200:203], v163 offset:55296
	ds_read_b128 v[204:207], v163 offset:56320
	global_load_lds_dwordx4 v146, s[98:99]
	s_add_i32 m0, s74, 0x2000
	s_add_u32 s38, s38, 0x40080
	s_addc_u32 s39, s39, 0
	s_add_i32 s74, s78, s33
	global_load_lds_dwordx4 v144, s[98:99]
	s_mov_b32 m0, s74
	s_nop 0
	global_load_lds_dwordx4 v146, s[38:39]
	s_add_i32 m0, s74, 0x2000
	s_nop 0
	global_load_lds_dwordx4 v144, s[38:39]
	s_mov_b32 m0, s53
	s_nop 0
	global_load_lds_dwordx4 v146, s[100:101]
	s_mov_b32 m0, s58
	s_nop 0
	global_load_lds_dwordx4 v144, s[100:101]
	s_waitcnt vmcnt(8)
	s_waitcnt lgkmcnt(0)
	s_barrier
	s_setprio 1
	s_waitcnt lgkmcnt(0)
	v_mfma_f32_16x16x32_bf16 v[60:63], v[128:131], v[172:175], v[60:63]
	v_mfma_f32_16x16x32_bf16 v[56:59], v[136:139], v[172:175], v[56:59]
	v_mfma_f32_16x16x32_bf16 v[44:47], v[128:131], v[180:183], v[44:47]
	v_mfma_f32_16x16x32_bf16 v[40:43], v[136:139], v[180:183], v[40:43]
	v_mfma_f32_16x16x32_bf16 v[36:39], v[128:131], v[188:191], v[36:39]
	v_mfma_f32_16x16x32_bf16 v[32:35], v[136:139], v[188:191], v[32:35]
	v_mfma_f32_16x16x32_bf16 v[20:23], v[128:131], v[200:203], v[20:23]
	v_mfma_f32_16x16x32_bf16 v[16:19], v[136:139], v[200:203], v[16:19]
	v_mfma_f32_16x16x32_bf16 v[60:63], v[132:135], v[176:179], v[60:63]
	v_mfma_f32_16x16x32_bf16 v[56:59], v[140:143], v[176:179], v[56:59]
	v_mfma_f32_16x16x32_bf16 v[44:47], v[132:135], v[184:187], v[44:47]
	v_mfma_f32_16x16x32_bf16 v[40:43], v[140:143], v[184:187], v[40:43]
	v_mfma_f32_16x16x32_bf16 v[36:39], v[132:135], v[192:195], v[36:39]
	v_mfma_f32_16x16x32_bf16 v[32:35], v[140:143], v[192:195], v[32:35]
	v_mfma_f32_16x16x32_bf16 v[20:23], v[132:135], v[204:207], v[20:23]
	v_mfma_f32_16x16x32_bf16 v[16:19], v[140:143], v[204:207], v[16:19]
	s_setprio 0
	s_setprio 1
	v_mfma_f32_16x16x32_bf16 v[52:55], v[152:155], v[172:175], v[52:55]
	v_mfma_f32_16x16x32_bf16 v[48:51], v[164:167], v[172:175], v[48:51]
	v_mfma_f32_16x16x32_bf16 v[28:31], v[152:155], v[180:183], v[28:31]
	v_mfma_f32_16x16x32_bf16 v[24:27], v[164:167], v[180:183], v[24:27]
	v_mfma_f32_16x16x32_bf16 v[12:15], v[152:155], v[188:191], v[12:15]
	v_mfma_f32_16x16x32_bf16 v[8:11], v[164:167], v[188:191], v[8:11]
	v_mfma_f32_16x16x32_bf16 v[4:7], v[152:155], v[200:203], v[4:7]
	v_mfma_f32_16x16x32_bf16 v[0:3], v[164:167], v[200:203], v[0:3]
	v_mfma_f32_16x16x32_bf16 v[52:55], v[156:159], v[176:179], v[52:55]
	v_mfma_f32_16x16x32_bf16 v[48:51], v[168:171], v[176:179], v[48:51]
	v_mfma_f32_16x16x32_bf16 v[28:31], v[156:159], v[184:187], v[28:31]
	v_mfma_f32_16x16x32_bf16 v[24:27], v[168:171], v[184:187], v[24:27]
	v_mfma_f32_16x16x32_bf16 v[12:15], v[156:159], v[192:195], v[12:15]
	v_mfma_f32_16x16x32_bf16 v[8:11], v[168:171], v[192:195], v[8:11]
	v_mfma_f32_16x16x32_bf16 v[4:7], v[156:159], v[204:207], v[4:7]
	v_mfma_f32_16x16x32_bf16 v[0:3], v[168:171], v[204:207], v[0:3]
	s_setprio 0
	s_barrier
	s_add_u32 s36, s36, 0x40080
	s_addc_u32 s37, s37, 0
	s_mov_b32 m0, s59
	s_nop 0
	global_load_lds_dwordx4 v146, s[36:37]
	s_mov_b32 m0, s60
	s_add_i32 s73, s73, 2
	global_load_lds_dwordx4 v144, s[36:37]
	s_add_u32 s69, s69, 0x100
	s_addc_u32 s70, s70, 0
	s_add_u32 s71, s71, 0x100
	s_addc_u32 s72, s72, 0
	s_cmp_gt_u32 s73, 13
	s_cbranch_scc0 .LBB0_775
	s_and_b64 vcc, exec, s[40:41]
	s_cbranch_vccz .LBB0_778
	s_barrier

; #define PG8_STAGE(bufoff, gbase, voff) do { _Pragma("unroll") for (int _i = 0; _i < 2; ++_i) \
;         __builtin_amdgcn_global_load_lds((const unsigned*)((const char*)(gbase) + (voff)[_i]), (LAS unsigned*)(lds + (bufoff) + ldsw + _i * 8192), 16, 0, 0); } while (0)
; #define PG8_LDA(dst, b, h) do { _Pragma("unroll") for (int m = 0; m < 4; ++m) _Pragma("unroll") for (int k = 0; k < 2; ++k) dst[m][k] = *(const LAS bf16x8*)(lds + PG8_SA(b, h) + aoff + m * 2048 + k * 1024); } while (0)
; #define PG8_LDB(dst, b, h) do { _Pragma("unroll") for (int n = 0; n < 2; ++n) _Pragma("unroll") for (int k = 0; k < 2; ++k) dst[n][k] = *(const LAS bf16x8*)(lds + PG8_SB(b, h) + boff + n * 2048 + k * 1024); } while (0)
; #define PG8_MMA(ai, bj, At, Bt_) do { __builtin_amdgcn_s_setprio(1); _Pragma("unroll") for (int m = 0; m < 4; ++m) _Pragma("unroll") for (int n = 0; n < 2; ++n) _Pragma("unroll") for (int k = 0; k < 2; ++k) \
;         acc[ai][bj][m][n] = __builtin_amdgcn_mfma_f32_16x16x32_bf16(Bt_[n][k], At[m][k], acc[ai][bj][m][n], 0, 0, 0); __builtin_amdgcn_s_setprio(0); } while (0)
; #define PG8_WAIT_L(n) asm volatile("s_waitcnt lgkmcnt(" #n ")" ::: "memory")
; #define PG8_WAIT_VR(rl) asm volatile("s_cmp_lg_u32 %0, 0\n\ts_cbranch_scc1 .Lwvr%=\n\ts_waitcnt vmcnt(8)\n.Lwvr%=:\n\ts_waitcnt vmcnt(24)" :: "s"(rl) : "scc", "memory")
; #define PG8_BAR __builtin_amdgcn_s_barrier()
; #define PG8_SCHED __builtin_amdgcn_sched_barrier(0)
; template <class Epi, class Sched, bool GATHER>
; __device__ __forceinline__ void gemm_phase(LAS unsigned char* lds, const int wid, const bf16_t* A, int lda, const bf16_t* Bt, int ldb, size_t b_estride, int K, const Sched& S, const Epi& E) {
;     ...
;             PG8_WAIT_VR(rl); PG8_WAIT_L(0); PG8_BAR; PG8_MMA(0, 0, At, B0); PG8_MMA(0, 1, At, B1); PG8_BAR; PG8_SCHED;
;             PG8_LDA(At, 0, 1); PG8_STAGE(PG8_SB(0, 0), b2, voffB); PG8_STAGE(PG8_SB(0, 1), b2 + hstepB, voffB); PG8_STAGE_A(PG8_SA(0, 0), a2, 0, k2, g20);
;             PG8_WAIT_VR(rl); PG8_WAIT_L(0); PG8_BAR; PG8_MMA(1, 0, At, B0); PG8_MMA(1, 1, At, B1); PG8_BAR; PG8_SCHED;
;             PG8_LDB(B0, 1, 0); PG8_LDB(B1, 1, 1); PG8_SCHED; PG8_LDA(At, 1, 0); PG8_STAGE_A(PG8_SA(0, 1), a2, 1, k2, g21);
.Lwvr15:
	s_waitcnt vmcnt(24)
	s_waitcnt lgkmcnt(0)
	s_barrier
	s_setprio 1
	s_waitcnt lgkmcnt(0)
	v_mfma_f32_16x16x32_bf16 v[124:127], v[144:147], v[192:195], v[124:127]
	v_mfma_f32_16x16x32_bf16 v[120:123], v[166:169], v[192:195], v[120:123]
	v_mfma_f32_16x16x32_bf16 v[108:111], v[144:147], v[200:203], v[108:111]
	v_mfma_f32_16x16x32_bf16 v[104:107], v[166:169], v[200:203], v[104:107]
	v_mfma_f32_16x16x32_bf16 v[92:95], v[144:147], v[208:211], v[92:95]
	v_mfma_f32_16x16x32_bf16 v[88:91], v[166:169], v[208:211], v[88:91]
	v_mfma_f32_16x16x32_bf16 v[76:79], v[144:147], v[216:219], v[76:79]
	v_mfma_f32_16x16x32_bf16 v[72:75], v[166:169], v[216:219], v[72:75]
	v_mfma_f32_16x16x32_bf16 v[124:127], v[160:163], v[196:199], v[124:127]
	v_mfma_f32_16x16x32_bf16 v[120:123], v[172:175], v[196:199], v[120:123]
	v_mfma_f32_16x16x32_bf16 v[108:111], v[160:163], v[204:207], v[108:111]
	v_mfma_f32_16x16x32_bf16 v[104:107], v[172:175], v[204:207], v[104:107]
	v_mfma_f32_16x16x32_bf16 v[92:95], v[160:163], v[212:215], v[92:95]
	v_mfma_f32_16x16x32_bf16 v[88:91], v[172:175], v[212:215], v[88:91]
	v_mfma_f32_16x16x32_bf16 v[76:79], v[160:163], v[220:223], v[76:79]
	v_mfma_f32_16x16x32_bf16 v[72:75], v[172:175], v[220:223], v[72:75]
	s_setprio 0
	s_setprio 1
	v_mfma_f32_16x16x32_bf16 v[116:119], v[176:179], v[192:195], v[116:119]
	v_mfma_f32_16x16x32_bf16 v[112:115], v[184:187], v[192:195], v[112:115]
	v_mfma_f32_16x16x32_bf16 v[100:103], v[176:179], v[200:203], v[100:103]
	v_mfma_f32_16x16x32_bf16 v[96:99], v[184:187], v[200:203], v[96:99]
	v_mfma_f32_16x16x32_bf16 v[84:87], v[176:179], v[208:211], v[84:87]
	v_mfma_f32_16x16x32_bf16 v[80:83], v[184:187], v[208:211], v[80:83]
	v_mfma_f32_16x16x32_bf16 v[68:71], v[176:179], v[216:219], v[68:71]
	v_mfma_f32_16x16x32_bf16 v[64:67], v[184:187], v[216:219], v[64:67]
	v_mfma_f32_16x16x32_bf16 v[116:119], v[180:183], v[196:199], v[116:119]
	v_mfma_f32_16x16x32_bf16 v[112:115], v[188:191], v[196:199], v[112:115]
	v_mfma_f32_16x16x32_bf16 v[100:103], v[180:183], v[204:207], v[100:103]
	v_mfma_f32_16x16x32_bf16 v[96:99], v[188:191], v[204:207], v[96:99]
	v_mfma_f32_16x16x32_bf16 v[84:87], v[180:183], v[212:215], v[84:87]
	v_mfma_f32_16x16x32_bf16 v[80:83], v[188:191], v[212:215], v[80:83]
	v_mfma_f32_16x16x32_bf16 v[68:71], v[180:183], v[220:223], v[68:71]
	v_mfma_f32_16x16x32_bf16 v[64:67], v[188:191], v[220:223], v[64:67]
	s_setprio 0
	s_barrier
	s_add_i32 s72, s52, s33
	s_add_u32 s98, s28, 0x80
	s_addc_u32 s99, s29, 0
	s_mov_b32 m0, s72
	ds_read_b128 v[192:195], v171 offset:16384
	ds_read_b128 v[196:199], v171 offset:17408
	ds_read_b128 v[200:203], v171 offset:18432
	ds_read_b128 v[204:207], v171 offset:19456
	ds_read_b128 v[208:211], v171 offset:20480
	ds_read_b128 v[212:215], v171 offset:21504
	ds_read_b128 v[216:219], v171 offset:22528
	ds_read_b128 v[220:223], v171 offset:23552
	global_load_lds_dwordx4 v130, s[28:29]
	s_add_i32 m0, s72, 0x2000
	s_add_u32 s72, s28, 0x20000
	s_addc_u32 s73, s29, 0
	s_add_i32 s74, s53, s33
	global_load_lds_dwordx4 v134, s[28:29]
	s_mov_b32 m0, s74
	s_add_u32 s100, s26, 0x80
	s_addc_u32 s101, s27, 0
	global_load_lds_dwordx4 v130, s[72:73]
	s_add_i32 m0, s74, 0x2000
	s_nop 0
	global_load_lds_dwordx4 v134, s[72:73]
	s_mov_b32 m0, s43
	s_nop 0
	global_load_lds_dwordx4 v128, s[26:27]
	s_mov_b32 m0, s44
	s_nop 0
	global_load_lds_dwordx4 v132, s[26:27]
	s_cmp_lg_u32 s71, 0
	s_cbranch_scc1 .Lwvr16
	s_waitcnt vmcnt(8)

; #define PG8_STAGE(bufoff, gbase, voff) do { _Pragma("unroll") for (int _i = 0; _i < 2; ++_i) \
;         __builtin_amdgcn_global_load_lds((const unsigned*)((const char*)(gbase) + (voff)[_i]), (LAS unsigned*)(lds + (bufoff) + ldsw + _i * 8192), 16, 0, 0); } while (0)
; #define PG8_LDA(dst, b, h) do { _Pragma("unroll") for (int m = 0; m < 4; ++m) _Pragma("unroll") for (int k = 0; k < 2; ++k) dst[m][k] = *(const LAS bf16x8*)(lds + PG8_SA(b, h) + aoff + m * 2048 + k * 1024); } while (0)
; #define PG8_MMA(ai, bj, At, Bt_) do { __builtin_amdgcn_s_setprio(1); _Pragma("unroll") for (int m = 0; m < 4; ++m) _Pragma("unroll") for (int n = 0; n < 2; ++n) _Pragma("unroll") for (int k = 0; k < 2; ++k) \
;         acc[ai][bj][m][n] = __builtin_amdgcn_mfma_f32_16x16x32_bf16(Bt_[n][k], At[m][k], acc[ai][bj][m][n], 0, 0, 0); __builtin_amdgcn_s_setprio(0); } while (0)
; #define PG8_WAIT_V(n) asm volatile("s_waitcnt vmcnt(" #n ")" ::: "memory")
; #define PG8_WAIT_L(n) asm volatile("s_waitcnt lgkmcnt(" #n ")" ::: "memory")
; #define PG8_WAIT_VR(rl) asm volatile("s_cmp_lg_u32 %0, 0\n\ts_cbranch_scc1 .Lwvr%=\n\ts_waitcnt vmcnt(8)\n.Lwvr%=:\n\ts_waitcnt vmcnt(24)" :: "s"(rl) : "scc", "memory")
; #define PG8_BAR __builtin_amdgcn_s_barrier()
; #define PG8_SCHED __builtin_amdgcn_sched_barrier(0)
; #define PG8_STAGE_A(bufoff, ptr_dense, half, ktoff, goffs) do { if constexpr (GATHER) { PG8_STAGE(bufoff, (const char*)A + (ktoff), goffs); } \
;         else { PG8_STAGE(bufoff, (ptr_dense) + (half) * hstepA, voffA); } } while (0)
; template <class Epi, class Sched, bool GATHER>
; __device__ __forceinline__ void gemm_phase(LAS unsigned char* lds, const int wid, const bf16_t* A, int lda, const bf16_t* Bt, int ldb, size_t b_estride, int K, const Sched& S, const Epi& E) {
;     ...
;             PG8_WAIT_VR(rl); PG8_WAIT_L(0); PG8_BAR; PG8_MMA(0, 0, At, B0); PG8_MMA(0, 1, At, B1); PG8_BAR; PG8_SCHED;
;             PG8_LDA(At, 1, 1); PG8_STAGE(PG8_SB(1, 0), b3, voffB); PG8_STAGE(PG8_SB(1, 1), b3 + hstepB, voffB); PG8_STAGE_A(PG8_SA(1, 0), a3, 0, k3, g20);
;             PG8_WAIT_V(8); PG8_WAIT_L(0); PG8_BAR; PG8_MMA(1, 0, At, B0); PG8_MMA(1, 1, At, B1); PG8_BAR; PG8_SCHED;
;             PG8_STAGE_A(PG8_SA(1, 1), a3, 1, k3, g21);
;         }
.Lwvr17:
	s_waitcnt vmcnt(24)
	s_waitcnt lgkmcnt(0)
	s_barrier
	s_setprio 1
	s_waitcnt lgkmcnt(0)
	v_mfma_f32_16x16x32_bf16 v[124:127], v[144:147], v[192:195], v[124:127]
	v_mfma_f32_16x16x32_bf16 v[120:123], v[166:169], v[192:195], v[120:123]
	v_mfma_f32_16x16x32_bf16 v[108:111], v[144:147], v[200:203], v[108:111]
	v_mfma_f32_16x16x32_bf16 v[104:107], v[166:169], v[200:203], v[104:107]
	v_mfma_f32_16x16x32_bf16 v[92:95], v[144:147], v[208:211], v[92:95]
	v_mfma_f32_16x16x32_bf16 v[88:91], v[166:169], v[208:211], v[88:91]
	v_mfma_f32_16x16x32_bf16 v[76:79], v[144:147], v[216:219], v[76:79]
	v_mfma_f32_16x16x32_bf16 v[72:75], v[166:169], v[216:219], v[72:75]
	v_mfma_f32_16x16x32_bf16 v[124:127], v[160:163], v[196:199], v[124:127]
	v_mfma_f32_16x16x32_bf16 v[120:123], v[172:175], v[196:199], v[120:123]
	v_mfma_f32_16x16x32_bf16 v[108:111], v[160:163], v[204:207], v[108:111]
	v_mfma_f32_16x16x32_bf16 v[104:107], v[172:175], v[204:207], v[104:107]
	v_mfma_f32_16x16x32_bf16 v[92:95], v[160:163], v[212:215], v[92:95]
	v_mfma_f32_16x16x32_bf16 v[88:91], v[172:175], v[212:215], v[88:91]
	v_mfma_f32_16x16x32_bf16 v[76:79], v[160:163], v[220:223], v[76:79]
	v_mfma_f32_16x16x32_bf16 v[72:75], v[172:175], v[220:223], v[72:75]
	s_setprio 0
	s_setprio 1
	v_mfma_f32_16x16x32_bf16 v[116:119], v[176:179], v[192:195], v[116:119]
	v_mfma_f32_16x16x32_bf16 v[112:115], v[184:187], v[192:195], v[112:115]
	v_mfma_f32_16x16x32_bf16 v[100:103], v[176:179], v[200:203], v[100:103]
	v_mfma_f32_16x16x32_bf16 v[96:99], v[184:187], v[200:203], v[96:99]
	v_mfma_f32_16x16x32_bf16 v[84:87], v[176:179], v[208:211], v[84:87]
	v_mfma_f32_16x16x32_bf16 v[80:83], v[184:187], v[208:211], v[80:83]
	v_mfma_f32_16x16x32_bf16 v[68:71], v[176:179], v[216:219], v[68:71]
	v_mfma_f32_16x16x32_bf16 v[64:67], v[184:187], v[216:219], v[64:67]
	v_mfma_f32_16x16x32_bf16 v[116:119], v[180:183], v[196:199], v[116:119]
	v_mfma_f32_16x16x32_bf16 v[112:115], v[188:191], v[196:199], v[112:115]
	v_mfma_f32_16x16x32_bf16 v[100:103], v[180:183], v[204:207], v[100:103]
	v_mfma_f32_16x16x32_bf16 v[96:99], v[188:191], v[204:207], v[96:99]
	v_mfma_f32_16x16x32_bf16 v[84:87], v[180:183], v[212:215], v[84:87]
	v_mfma_f32_16x16x32_bf16 v[80:83], v[188:191], v[212:215], v[80:83]
	v_mfma_f32_16x16x32_bf16 v[68:71], v[180:183], v[220:223], v[68:71]
	v_mfma_f32_16x16x32_bf16 v[64:67], v[188:191], v[220:223], v[64:67]
	s_setprio 0
	s_barrier
	s_add_i32 s71, s74, s33
	s_mov_b32 m0, s71
	ds_read_b128 v[192:195], v171 offset:49152
	ds_read_b128 v[196:199], v171 offset:50176
	ds_read_b128 v[200:203], v171 offset:51200
	ds_read_b128 v[204:207], v171 offset:52224
	ds_read_b128 v[208:211], v171 offset:53248
	ds_read_b128 v[212:215], v171 offset:54272
	ds_read_b128 v[216:219], v171 offset:55296
	ds_read_b128 v[220:223], v171 offset:56320
	global_load_lds_dwordx4 v130, s[98:99]
	s_add_i32 m0, s71, 0x2000
	s_add_u32 s28, s28, 0x20080
	s_addc_u32 s29, s29, 0
	s_add_i32 s71, s75, s33
	global_load_lds_dwordx4 v134, s[98:99]
	s_mov_b32 m0, s71
	s_nop 0
	global_load_lds_dwordx4 v130, s[28:29]
	s_add_i32 m0, s71, 0x2000
	s_nop 0
	global_load_lds_dwordx4 v134, s[28:29]
	s_mov_b32 m0, s38
	s_nop 0
	global_load_lds_dwordx4 v128, s[100:101]
	s_mov_b32 m0, s39
	s_nop 0
	global_load_lds_dwordx4 v132, s[100:101]
	s_waitcnt vmcnt(8)
	s_waitcnt lgkmcnt(0)
	s_barrier
	s_setprio 1
	s_waitcnt lgkmcnt(0)
	v_mfma_f32_16x16x32_bf16 v[60:63], v[144:147], v[192:195], v[60:63]
	v_mfma_f32_16x16x32_bf16 v[56:59], v[166:169], v[192:195], v[56:59]
	v_mfma_f32_16x16x32_bf16 v[44:47], v[144:147], v[200:203], v[44:47]
	v_mfma_f32_16x16x32_bf16 v[40:43], v[166:169], v[200:203], v[40:43]
	v_mfma_f32_16x16x32_bf16 v[28:31], v[144:147], v[208:211], v[28:31]
	v_mfma_f32_16x16x32_bf16 v[24:27], v[166:169], v[208:211], v[24:27]
	v_mfma_f32_16x16x32_bf16 v[12:15], v[144:147], v[216:219], v[12:15]
	v_mfma_f32_16x16x32_bf16 v[8:11], v[166:169], v[216:219], v[8:11]
	v_mfma_f32_16x16x32_bf16 v[60:63], v[160:163], v[196:199], v[60:63]
	v_mfma_f32_16x16x32_bf16 v[56:59], v[172:175], v[196:199], v[56:59]
	v_mfma_f32_16x16x32_bf16 v[44:47], v[160:163], v[204:207], v[44:47]
	v_mfma_f32_16x16x32_bf16 v[40:43], v[172:175], v[204:207], v[40:43]
	v_mfma_f32_16x16x32_bf16 v[28:31], v[160:163], v[212:215], v[28:31]
	v_mfma_f32_16x16x32_bf16 v[24:27], v[172:175], v[212:215], v[24:27]
	v_mfma_f32_16x16x32_bf16 v[12:15], v[160:163], v[220:223], v[12:15]
	v_mfma_f32_16x16x32_bf16 v[8:11], v[172:175], v[220:223], v[8:11]
	s_setprio 0
	s_setprio 1
	v_mfma_f32_16x16x32_bf16 v[52:55], v[176:179], v[192:195], v[52:55]
	v_mfma_f32_16x16x32_bf16 v[48:51], v[184:187], v[192:195], v[48:51]
	v_mfma_f32_16x16x32_bf16 v[36:39], v[176:179], v[200:203], v[36:39]
	v_mfma_f32_16x16x32_bf16 v[32:35], v[184:187], v[200:203], v[32:35]
	v_mfma_f32_16x16x32_bf16 v[20:23], v[176:179], v[208:211], v[20:23]
	v_mfma_f32_16x16x32_bf16 v[16:19], v[184:187], v[208:211], v[16:19]
	v_mfma_f32_16x16x32_bf16 v[4:7], v[176:179], v[216:219], v[4:7]
	v_mfma_f32_16x16x32_bf16 v[0:3], v[184:187], v[216:219], v[0:3]
	v_mfma_f32_16x16x32_bf16 v[52:55], v[180:183], v[196:199], v[52:55]
	v_mfma_f32_16x16x32_bf16 v[48:51], v[188:191], v[196:199], v[48:51]
	v_mfma_f32_16x16x32_bf16 v[36:39], v[180:183], v[204:207], v[36:39]
	v_mfma_f32_16x16x32_bf16 v[32:35], v[188:191], v[204:207], v[32:35]
	v_mfma_f32_16x16x32_bf16 v[20:23], v[180:183], v[212:215], v[20:23]
	v_mfma_f32_16x16x32_bf16 v[16:19], v[188:191], v[212:215], v[16:19]
	v_mfma_f32_16x16x32_bf16 v[4:7], v[180:183], v[220:223], v[4:7]
	v_mfma_f32_16x16x32_bf16 v[0:3], v[188:191], v[220:223], v[0:3]
	s_setprio 0
	s_barrier
	s_add_u32 s26, s26, 0x20080
	s_addc_u32 s27, s27, 0
	s_mov_b32 m0, s47
	s_nop 0
	global_load_lds_dwordx4 v128, s[26:27]
	s_mov_b32 m0, s51
	s_add_i32 s70, s70, 2
	global_load_lds_dwordx4 v132, s[26:27]
	s_add_u32 s66, s66, 0x100
	s_addc_u32 s67, s67, 0
	s_add_u32 s68, s68, 0x100
	s_addc_u32 s69, s69, 0
	s_cmp_gt_u32 s70, 5
	s_cbranch_scc0 .LBB0_1202
	s_and_b64 vcc, exec, s[40:41]
	s_cbranch_vccz .LBB0_1205
	s_barrier
